# K1: wave-to-d-chunk assignment rotated by code-group index so the 8 workgroups sharing an x slab request different chunks at the same time (x loads become L2 hits)
# speedup vs baseline: 1.0211x; 1.0211x over previous
.LBB0_6:
	s_or_saveexec_b64 s[14:15], s[4:5]
	v_and_b32_e32 v194, 63, v0
	s_bfe_u32 s17, s2, 0x30003
	v_mov_b32_e32 v195, 0
	v_mov_b32_e32 v58, 0
	v_mov_b32_e32 v59, 0
	v_mov_b32_e32 v60, 0
	v_mov_b32_e32 v61, 0
	v_mov_b32_e32 v62, 0
	v_mov_b32_e32 v63, 0
	v_mov_b32_e32 v64, 0
	v_mov_b32_e32 v65, 0
	v_mov_b32_e32 v74, 0
	v_mov_b32_e32 v75, 0
	v_mov_b32_e32 v76, 0
	v_mov_b32_e32 v77, 0
	v_mov_b32_e32 v78, 0
	v_mov_b32_e32 v79, 0
	v_mov_b32_e32 v80, 0
	v_mov_b32_e32 v81, 0
	v_mov_b32_e32 v82, 0
	v_mov_b32_e32 v83, 0
	v_mov_b32_e32 v84, 0
	v_mov_b32_e32 v85, 0
	v_mov_b32_e32 v86, 0
	v_mov_b32_e32 v87, 0
	v_mov_b32_e32 v88, 0
	v_mov_b32_e32 v89, 0
	v_mov_b32_e32 v90, 0
	v_mov_b32_e32 v91, 0
	v_mov_b32_e32 v92, 0
	v_mov_b32_e32 v93, 0
	v_mov_b32_e32 v94, 0
	v_mov_b32_e32 v95, 0
	v_mov_b32_e32 v96, 0
	v_mov_b32_e32 v97, 0
	v_mov_b32_e32 v98, 0
	v_mov_b32_e32 v99, 0
	v_mov_b32_e32 v100, 0
	v_mov_b32_e32 v101, 0
	v_mov_b32_e32 v102, 0
	v_mov_b32_e32 v103, 0
	v_mov_b32_e32 v104, 0
	v_mov_b32_e32 v105, 0
	v_mov_b32_e32 v106, 0
	v_mov_b32_e32 v107, 0
	v_mov_b32_e32 v108, 0
	v_mov_b32_e32 v109, 0
	v_mov_b32_e32 v110, 0
	v_mov_b32_e32 v111, 0
	v_mov_b32_e32 v112, 0
	v_mov_b32_e32 v113, 0
	v_mov_b32_e32 v114, 0
	v_mov_b32_e32 v115, 0
	v_mov_b32_e32 v116, 0
	v_mov_b32_e32 v117, 0
	v_mov_b32_e32 v118, 0
	v_mov_b32_e32 v119, 0
	v_mov_b32_e32 v120, 0
	v_mov_b32_e32 v121, 0
	v_mov_b32_e32 v2, 0
	v_mov_b32_e32 v3, 0
	v_mov_b32_e32 v4, 0
	v_mov_b32_e32 v5, 0
	v_mov_b32_e32 v6, 0
	v_mov_b32_e32 v7, 0
	v_mov_b32_e32 v8, 0
	v_mov_b32_e32 v9, 0
	s_xor_b64 exec, exec, s[14:15]
	s_cbranch_execz .LBB0_8
	s_cmp_lt_u32 s16, 26
	s_cselect_b32 s26, 8, 7
	v_add_u32_e32 v242, s17, v1
	v_subrev_u32_e32 v243, s26, v242
	v_cmp_le_u32_e32 vcc, s26, v242
	s_nop 1
	v_cndmask_b32_e32 v242, v242, v243, vcc
	v_add_lshl_u32 v36, s3, v242, 7
	v_mul_u32_u24_e32 v82, 0x1f400, v130
	v_mov_b32_e32 v83, 0
	v_ashrrev_i32_e32 v37, 31, v36
	s_waitcnt lgkmcnt(0)
	v_lshl_add_u64 v[2:3], s[20:21], 0, v[82:83]
	v_lshl_add_u64 v[2:3], v[36:37], 2, v[2:3]
	v_and_b32_e32 v82, 48, v194
	v_lshl_add_u64 v[2:3], v[2:3], 0, v[82:83]
	s_mov_b32 s2, 0x1f4000
	v_add_co_u32_e32 v240, vcc, s2, v2
	v_lshrrev_b32_e32 v83, 4, v194
	s_nop 0
	v_addc_co_u32_e32 v241, vcc, 0, v3, vcc
	global_load_dwordx4 v[166:169], v[2:3], off
	global_load_dwordx4 v[170:173], v[2:3], off offset:64
	global_load_dwordx4 v[174:177], v[2:3], off offset:128
	global_load_dwordx4 v[178:181], v[2:3], off offset:192
	global_load_dwordx4 v[182:185], v[2:3], off offset:256
	global_load_dwordx4 v[186:189], v[2:3], off offset:320
	global_load_dwordx4 v[190:193], v[2:3], off offset:384
	global_load_dwordx4 v[204:207], v[2:3], off offset:448
	global_load_dwordx4 v[208:211], v[240:241], off
	global_load_dwordx4 v[212:215], v[240:241], off offset:64
	global_load_dwordx4 v[216:219], v[240:241], off offset:128
	global_load_dwordx4 v[220:223], v[240:241], off offset:192
	global_load_dwordx4 v[224:227], v[240:241], off offset:256
	global_load_dwordx4 v[228:231], v[240:241], off offset:320
	global_load_dwordx4 v[232:235], v[240:241], off offset:384
	global_load_dwordx4 v[236:239], v[240:241], off offset:448
	v_lshl_or_b32 v37, s17, 7, v83
	s_movk_i32 s3, 0x7d00
	v_mad_u32_u24 v36, v37, s3, v36
	v_lshlrev_b32_e32 v96, 4, v130
	s_and_b32 s9, s23, 0xffff
	s_mov_b32 s11, 0x20000
	s_mov_b32 s10, 0x7d00000
	s_mov_b32 s8, s22
	v_lshl_or_b32 v201, v36, 2, v96
	s_mov_b32 s3, 0x7d000
	buffer_load_dwordx4 v[122:125], v201, s[8:11], s3 offen nt
	s_mov_b32 s4, 0xfa000
	buffer_load_dwordx4 v[126:129], v201, s[8:11], s4 offen nt
	s_mov_b32 s3, 0x177000
	buffer_load_dwordx4 v[132:135], v201, s[8:11], s3 offen nt
	s_mov_b32 s4, 0x100
	buffer_load_dwordx4 v[136:139], v201, s[8:11], s4 offen nt
	s_mov_b32 s3, 0x7d100
	buffer_load_dwordx4 v[140:143], v201, s[8:11], s3 offen nt
	s_mov_b32 s4, 0xfa100
	buffer_load_dwordx4 v[154:157], v201, s[8:11], s4 offen nt
	buffer_load_dwordx4 v[158:161], v201, s[8:11], 0 offen nt
	s_mov_b32 s4, 0x1f4000
	buffer_load_dwordx4 v[58:61], v201, s[8:11], s4 offen nt
	s_mov_b32 s3, 0x177100
	buffer_load_dwordx4 v[162:165], v201, s[8:11], s3 offen nt
	s_mov_b32 s4, 0x271000
	buffer_load_dwordx4 v[62:65], v201, s[8:11], s4 offen nt
	s_mov_b32 s3, 0x2ee000
	buffer_load_dwordx4 v[98:101], v201, s[8:11], s3 offen nt
	s_mov_b32 s4, 0x36b000
	buffer_load_dwordx4 v[102:105], v201, s[8:11], s4 offen nt
	s_mov_b32 s3, 0x1f4100
	buffer_load_dwordx4 v[106:109], v201, s[8:11], s3 offen nt
	s_mov_b32 s4, 0x271100
	buffer_load_dwordx4 v[110:113], v201, s[8:11], s4 offen nt
	s_mov_b32 s3, 0x2ee100
	buffer_load_dwordx4 v[146:149], v201, s[8:11], s3 offen nt
	s_mov_b32 s4, 0x36b100
	buffer_load_dwordx4 v[150:153], v201, s[8:11], s4 offen nt
	s_mov_b32 s3, 0x3e8000
	buffer_load_dwordx4 v[74:77], v201, s[8:11], s3 offen nt
	s_mov_b32 s4, 0x465000
	buffer_load_dwordx4 v[78:81], v201, s[8:11], s4 offen nt
	s_mov_b32 s3, 0x4e2000
	buffer_load_dwordx4 v[114:117], v201, s[8:11], s3 offen nt
	s_mov_b32 s4, 0x55f000
	buffer_load_dwordx4 v[118:121], v201, s[8:11], s4 offen nt
	v_mul_u32_u24_e32 v86, 0x120, v130
	v_mul_u32_u24_e32 v84, 0x2400, v1
	v_mul_u32_u24_e32 v85, 0x120, v83
	v_add3_u32 v200, v84, v85, v96
	s_waitcnt vmcnt(34)
	v_cvt_pk_bf16_f32 v22, v166, v167
	v_cvt_pk_bf16_f32 v23, v168, v169
	v_cvt_pk_bf16_f32 v24, v170, v171
	v_cvt_pk_bf16_f32 v25, v172, v173
	v_lshlrev_b32_e32 v242, 16, v22
	v_and_b32_e32 v243, 0xffff0000, v22
	v_lshlrev_b32_e32 v244, 16, v23
	v_and_b32_e32 v245, 0xffff0000, v23
	v_lshlrev_b32_e32 v246, 16, v24
	v_and_b32_e32 v247, 0xffff0000, v24
	v_lshlrev_b32_e32 v248, 16, v25
	v_and_b32_e32 v249, 0xffff0000, v25
	v_pk_add_f32 v[242:243], v[166:167], v[242:243] neg_lo:[0,1] neg_hi:[0,1]
	v_pk_add_f32 v[244:245], v[168:169], v[244:245] neg_lo:[0,1] neg_hi:[0,1]
	v_pk_add_f32 v[246:247], v[170:171], v[246:247] neg_lo:[0,1] neg_hi:[0,1]
	v_pk_add_f32 v[248:249], v[172:173], v[248:249] neg_lo:[0,1] neg_hi:[0,1]
	v_cvt_pk_bf16_f32 v30, v242, v243
	v_cvt_pk_bf16_f32 v31, v244, v245
	v_cvt_pk_bf16_f32 v32, v246, v247
	v_cvt_pk_bf16_f32 v33, v248, v249
	s_waitcnt vmcnt(32)
	v_cvt_pk_bf16_f32 v18, v174, v175
	v_cvt_pk_bf16_f32 v19, v176, v177
	v_cvt_pk_bf16_f32 v20, v178, v179
	v_cvt_pk_bf16_f32 v21, v180, v181
	v_lshlrev_b32_e32 v242, 16, v18
	v_and_b32_e32 v243, 0xffff0000, v18
	v_lshlrev_b32_e32 v244, 16, v19
	v_and_b32_e32 v245, 0xffff0000, v19
	v_lshlrev_b32_e32 v246, 16, v20
	v_and_b32_e32 v247, 0xffff0000, v20
	v_lshlrev_b32_e32 v248, 16, v21
	v_and_b32_e32 v249, 0xffff0000, v21
	v_pk_add_f32 v[242:243], v[174:175], v[242:243] neg_lo:[0,1] neg_hi:[0,1]
	v_pk_add_f32 v[244:245], v[176:177], v[244:245] neg_lo:[0,1] neg_hi:[0,1]
	v_pk_add_f32 v[246:247], v[178:179], v[246:247] neg_lo:[0,1] neg_hi:[0,1]
	v_pk_add_f32 v[248:249], v[180:181], v[248:249] neg_lo:[0,1] neg_hi:[0,1]
	v_cvt_pk_bf16_f32 v26, v242, v243
	v_cvt_pk_bf16_f32 v27, v244, v245
	v_cvt_pk_bf16_f32 v28, v246, v247
	v_cvt_pk_bf16_f32 v29, v248, v249
	s_waitcnt vmcnt(30)
	v_cvt_pk_bf16_f32 v6, v182, v183
	v_cvt_pk_bf16_f32 v7, v184, v185
	v_cvt_pk_bf16_f32 v8, v186, v187
	v_cvt_pk_bf16_f32 v9, v188, v189
	v_lshlrev_b32_e32 v242, 16, v6
	v_and_b32_e32 v243, 0xffff0000, v6
	v_lshlrev_b32_e32 v244, 16, v7
	v_and_b32_e32 v245, 0xffff0000, v7
	v_lshlrev_b32_e32 v246, 16, v8
	v_and_b32_e32 v247, 0xffff0000, v8
	v_lshlrev_b32_e32 v248, 16, v9
	v_and_b32_e32 v249, 0xffff0000, v9
	v_pk_add_f32 v[242:243], v[182:183], v[242:243] neg_lo:[0,1] neg_hi:[0,1]
	v_pk_add_f32 v[244:245], v[184:185], v[244:245] neg_lo:[0,1] neg_hi:[0,1]
	v_pk_add_f32 v[246:247], v[186:187], v[246:247] neg_lo:[0,1] neg_hi:[0,1]
	v_pk_add_f32 v[248:249], v[188:189], v[248:249] neg_lo:[0,1] neg_hi:[0,1]
	v_cvt_pk_bf16_f32 v14, v242, v243
	v_cvt_pk_bf16_f32 v15, v244, v245
	v_cvt_pk_bf16_f32 v16, v246, v247
	v_cvt_pk_bf16_f32 v17, v248, v249
	s_waitcnt vmcnt(28)
	v_cvt_pk_bf16_f32 v2, v190, v191
	v_cvt_pk_bf16_f32 v3, v192, v193
	v_cvt_pk_bf16_f32 v4, v204, v205
	v_cvt_pk_bf16_f32 v5, v206, v207
	v_lshlrev_b32_e32 v242, 16, v2
	v_and_b32_e32 v243, 0xffff0000, v2
	v_lshlrev_b32_e32 v244, 16, v3
	v_and_b32_e32 v245, 0xffff0000, v3
	v_lshlrev_b32_e32 v246, 16, v4
	v_and_b32_e32 v247, 0xffff0000, v4
	v_lshlrev_b32_e32 v248, 16, v5
	v_and_b32_e32 v249, 0xffff0000, v5
	v_pk_add_f32 v[242:243], v[190:191], v[242:243] neg_lo:[0,1] neg_hi:[0,1]
	v_pk_add_f32 v[244:245], v[192:193], v[244:245] neg_lo:[0,1] neg_hi:[0,1]
	v_pk_add_f32 v[246:247], v[204:205], v[246:247] neg_lo:[0,1] neg_hi:[0,1]
	v_pk_add_f32 v[248:249], v[206:207], v[248:249] neg_lo:[0,1] neg_hi:[0,1]
	v_cvt_pk_bf16_f32 v10, v242, v243
	v_cvt_pk_bf16_f32 v11, v244, v245
	v_cvt_pk_bf16_f32 v12, v246, v247
	v_cvt_pk_bf16_f32 v13, v248, v249
	s_waitcnt vmcnt(26)
	v_cvt_pk_bf16_f32 v34, v208, v209
	v_cvt_pk_bf16_f32 v35, v210, v211
	v_cvt_pk_bf16_f32 v36, v212, v213
	v_cvt_pk_bf16_f32 v37, v214, v215
	v_lshlrev_b32_e32 v242, 16, v34
	v_and_b32_e32 v243, 0xffff0000, v34
	v_lshlrev_b32_e32 v244, 16, v35
	v_and_b32_e32 v245, 0xffff0000, v35
	v_lshlrev_b32_e32 v246, 16, v36
	v_and_b32_e32 v247, 0xffff0000, v36
	v_lshlrev_b32_e32 v248, 16, v37
	v_and_b32_e32 v249, 0xffff0000, v37
	v_pk_add_f32 v[242:243], v[208:209], v[242:243] neg_lo:[0,1] neg_hi:[0,1]
	v_pk_add_f32 v[244:245], v[210:211], v[244:245] neg_lo:[0,1] neg_hi:[0,1]
	v_pk_add_f32 v[246:247], v[212:213], v[246:247] neg_lo:[0,1] neg_hi:[0,1]
	v_pk_add_f32 v[248:249], v[214:215], v[248:249] neg_lo:[0,1] neg_hi:[0,1]
	v_cvt_pk_bf16_f32 v38, v242, v243
	v_cvt_pk_bf16_f32 v39, v244, v245
	v_cvt_pk_bf16_f32 v40, v246, v247
	v_cvt_pk_bf16_f32 v41, v248, v249
	s_waitcnt vmcnt(24)
	v_cvt_pk_bf16_f32 v66, v216, v217
	v_cvt_pk_bf16_f32 v67, v218, v219
	v_cvt_pk_bf16_f32 v68, v220, v221
	v_cvt_pk_bf16_f32 v69, v222, v223
	v_lshlrev_b32_e32 v242, 16, v66
	v_and_b32_e32 v243, 0xffff0000, v66
	v_lshlrev_b32_e32 v244, 16, v67
	v_and_b32_e32 v245, 0xffff0000, v67
	v_lshlrev_b32_e32 v246, 16, v68
	v_and_b32_e32 v247, 0xffff0000, v68
	v_lshlrev_b32_e32 v248, 16, v69
	v_and_b32_e32 v249, 0xffff0000, v69
	v_pk_add_f32 v[242:243], v[216:217], v[242:243] neg_lo:[0,1] neg_hi:[0,1]
	v_pk_add_f32 v[244:245], v[218:219], v[244:245] neg_lo:[0,1] neg_hi:[0,1]
	v_pk_add_f32 v[246:247], v[220:221], v[246:247] neg_lo:[0,1] neg_hi:[0,1]
	v_pk_add_f32 v[248:249], v[222:223], v[248:249] neg_lo:[0,1] neg_hi:[0,1]
	v_cvt_pk_bf16_f32 v70, v242, v243
	v_cvt_pk_bf16_f32 v71, v244, v245
	v_cvt_pk_bf16_f32 v72, v246, v247
	v_cvt_pk_bf16_f32 v73, v248, v249
	s_waitcnt vmcnt(22)
	v_cvt_pk_bf16_f32 v50, v224, v225
	v_cvt_pk_bf16_f32 v51, v226, v227
	v_cvt_pk_bf16_f32 v52, v228, v229
	v_cvt_pk_bf16_f32 v53, v230, v231
	v_lshlrev_b32_e32 v242, 16, v50
	v_and_b32_e32 v243, 0xffff0000, v50
	v_lshlrev_b32_e32 v244, 16, v51
	v_and_b32_e32 v245, 0xffff0000, v51
	v_lshlrev_b32_e32 v246, 16, v52
	v_and_b32_e32 v247, 0xffff0000, v52
	v_lshlrev_b32_e32 v248, 16, v53
	v_and_b32_e32 v249, 0xffff0000, v53
	v_pk_add_f32 v[242:243], v[224:225], v[242:243] neg_lo:[0,1] neg_hi:[0,1]
	v_pk_add_f32 v[244:245], v[226:227], v[244:245] neg_lo:[0,1] neg_hi:[0,1]
	v_pk_add_f32 v[246:247], v[228:229], v[246:247] neg_lo:[0,1] neg_hi:[0,1]
	v_pk_add_f32 v[248:249], v[230:231], v[248:249] neg_lo:[0,1] neg_hi:[0,1]
	v_cvt_pk_bf16_f32 v54, v242, v243
	v_cvt_pk_bf16_f32 v55, v244, v245
	v_cvt_pk_bf16_f32 v56, v246, v247
	v_cvt_pk_bf16_f32 v57, v248, v249
	s_waitcnt vmcnt(20)
	v_cvt_pk_bf16_f32 v42, v232, v233
	v_cvt_pk_bf16_f32 v43, v234, v235
	v_cvt_pk_bf16_f32 v44, v236, v237
	v_cvt_pk_bf16_f32 v45, v238, v239
	v_lshlrev_b32_e32 v242, 16, v42
	v_and_b32_e32 v243, 0xffff0000, v42
	v_lshlrev_b32_e32 v244, 16, v43
	v_and_b32_e32 v245, 0xffff0000, v43
	v_lshlrev_b32_e32 v246, 16, v44
	v_and_b32_e32 v247, 0xffff0000, v44
	v_lshlrev_b32_e32 v248, 16, v45
	v_and_b32_e32 v249, 0xffff0000, v45
	v_pk_add_f32 v[242:243], v[232:233], v[242:243] neg_lo:[0,1] neg_hi:[0,1]
	v_pk_add_f32 v[244:245], v[234:235], v[244:245] neg_lo:[0,1] neg_hi:[0,1]
	v_pk_add_f32 v[246:247], v[236:237], v[246:247] neg_lo:[0,1] neg_hi:[0,1]
	v_pk_add_f32 v[248:249], v[238:239], v[248:249] neg_lo:[0,1] neg_hi:[0,1]
	v_cvt_pk_bf16_f32 v46, v242, v243
	v_cvt_pk_bf16_f32 v47, v244, v245
	v_cvt_pk_bf16_f32 v48, v246, v247
	v_cvt_pk_bf16_f32 v49, v248, v249
	s_waitcnt vmcnt(13)
	ds_write_b128 v200, v[158:161]
	ds_write_b128 v200, v[122:125] offset:1152
	ds_write_b128 v200, v[126:129] offset:2304
	ds_write_b128 v200, v[132:135] offset:3456
	v_add3_u32 v197, v84, v86, v82
	ds_read_b128 v[90:93], v197
	ds_read_b128 v[94:97], v197 offset:64
	ds_read_b128 v[132:135], v197 offset:128
	ds_read_b128 v[158:161], v197 offset:192
	v_lshrrev_b32_e32 v82, 2, v130
	v_and_b32_e32 v84, 3, v0
	v_cmp_eq_u32_e32 vcc, v83, v82
	v_or_b32_e32 v196, 0x800, v0
	s_nop 0
	v_cndmask_b32_e32 v82, 4, v84, vcc
	v_cmp_eq_u32_e64 s[6:7], 0, v82
	v_cmp_eq_u32_e64 s[4:5], 1, v82
	v_cmp_eq_u32_e64 s[2:3], 2, v82
	v_cmp_eq_u32_e32 vcc, 3, v82
	s_mov_b32 s18, 0x3e8100
	s_mov_b32 s19, 0x465100
	buffer_load_dwordx4 v[82:85], v201, s[8:11], s18 offen nt
	buffer_load_dwordx4 v[86:89], v201, s[8:11], s19 offen nt
	s_mov_b32 s18, 0x4e2100
	s_mov_b32 s19, 0x55f100
	buffer_load_dwordx4 v[122:125], v201, s[8:11], s18 offen nt
	buffer_load_dwordx4 v[126:129], v201, s[8:11], s19 offen nt
	ds_write_b128 v200, v[136:139] offset:4608
	ds_write_b128 v200, v[140:143] offset:5760
	ds_write_b128 v200, v[154:157] offset:6912
	s_waitcnt vmcnt(15)
	ds_write_b128 v200, v[162:165] offset:8064
	s_waitcnt lgkmcnt(7)
	v_cvt_pk_bf16_f32 v136, v90, v91
	v_cvt_pk_bf16_f32 v137, v92, v93
	s_waitcnt lgkmcnt(6)
	v_cvt_pk_bf16_f32 v138, v94, v95
	v_cvt_pk_bf16_f32 v139, v96, v97
	v_lshlrev_b32_e32 v144, 16, v136
	v_and_b32_e32 v145, 0xffff0000, v136
	v_mfma_f32_16x16x32_bf16 v[140:143], v[22:25], v[136:139], 0
	v_add_f32_e64 v90, v90, -v144
	v_add_f32_e64 v91, v91, -v145
	v_lshlrev_b32_e32 v144, 16, v137
	v_and_b32_e32 v145, 0xffff0000, v137
	v_mfma_f32_16x16x32_bf16 v[154:157], v[34:37], v[136:139], 0
	v_add_f32_e64 v92, v92, -v144
	v_add_f32_e64 v93, v93, -v145
	v_cvt_pk_bf16_f32 v90, v90, v91
	v_cvt_pk_bf16_f32 v91, v92, v93
	v_lshlrev_b32_e32 v92, 16, v138
	v_and_b32_e32 v93, 0xffff0000, v138
	v_mfma_f32_16x16x32_bf16 v[140:143], v[30:33], v[136:139], v[140:143]
	v_add_f32_e64 v92, v94, -v92
	v_add_f32_e64 v93, v95, -v93
	v_lshlrev_b32_e32 v94, 16, v139
	v_and_b32_e32 v95, 0xffff0000, v139
	v_mfma_f32_16x16x32_bf16 v[154:157], v[38:41], v[136:139], v[154:157]
	v_add_f32_e64 v94, v96, -v94
	v_add_f32_e64 v95, v97, -v95
	v_cvt_pk_bf16_f32 v92, v92, v93
	v_cvt_pk_bf16_f32 v93, v94, v95
	v_mfma_f32_16x16x32_bf16 v[162:165], v[136:139], v[136:139], 0
	v_lshl_or_b32 v199, v1, 8, v130
	v_cndmask_b32_e64 v130, v196, v199, s[6:7]
	v_mov_b32_e32 v198, 0x20000
	v_mfma_f32_16x16x32_bf16 v[94:97], v[136:139], v[90:93], 0
	v_lshl_or_b32 v130, v130, 2, v198
	v_mfma_f32_16x16x32_bf16 v[136:139], v[22:25], v[90:93], v[140:143]
	v_mfma_f32_16x16x32_bf16 v[90:93], v[34:37], v[90:93], v[154:157]
	s_waitcnt lgkmcnt(5)
	s_nop 0
	v_cvt_pk_bf16_f32 v140, v132, v133
	v_lshlrev_b32_e32 v142, 16, v140
	v_and_b32_e32 v143, 0xffff0000, v140
	v_pk_add_f32 v[132:133], v[132:133], v[142:143] neg_lo:[0,1] neg_hi:[0,1]
	v_cvt_pk_bf16_f32 v141, v134, v135
	s_waitcnt lgkmcnt(4)
	v_cvt_pk_bf16_f32 v142, v158, v159
	v_cvt_pk_bf16_f32 v143, v160, v161
	v_lshlrev_b32_e32 v144, 16, v141
	v_and_b32_e32 v145, 0xffff0000, v141
	v_mfma_f32_16x16x32_bf16 v[90:93], v[66:69], v[140:143], v[90:93]
	v_add_f32_e64 v134, v134, -v144
	v_add_f32_e64 v135, v135, -v145
	v_cvt_pk_bf16_f32 v132, v132, v133
	v_cvt_pk_bf16_f32 v133, v134, v135
	v_lshlrev_b32_e32 v134, 16, v142
	v_and_b32_e32 v135, 0xffff0000, v142
	v_lshlrev_b32_e32 v144, 16, v143
	v_and_b32_e32 v145, 0xffff0000, v143
	v_pk_add_f32 v[134:135], v[158:159], v[134:135] neg_lo:[0,1] neg_hi:[0,1]
	v_pk_add_f32 v[144:145], v[160:161], v[144:145] neg_lo:[0,1] neg_hi:[0,1]
	v_mfma_f32_16x16x32_bf16 v[136:139], v[18:21], v[140:143], v[136:139]
	v_cvt_pk_bf16_f32 v134, v134, v135
	v_cvt_pk_bf16_f32 v135, v144, v145
	v_mfma_f32_16x16x32_bf16 v[90:93], v[70:73], v[140:143], v[90:93]
	v_mfma_f32_16x16x32_bf16 v[154:157], v[140:143], v[140:143], v[162:165]
	v_mfma_f32_16x16x32_bf16 v[94:97], v[140:143], v[132:135], v[94:97]
	v_mfma_f32_16x16x32_bf16 v[136:139], v[26:29], v[140:143], v[136:139]
	v_mfma_f32_16x16x32_bf16 v[142:145], v[66:69], v[132:135], v[90:93]
	s_nop 5
	v_fma_f32 v94, v94, 2.0, v154
	v_fma_f32 v95, v95, 2.0, v155
	ds_write_b32 v130, v94
	v_pk_fma_f32 v[96:97], v[96:97], 2.0, v[156:157] op_sel_hi:[1,0,1]
	v_cndmask_b32_e64 v90, v196, v199, s[4:5]
	v_lshl_or_b32 v90, v90, 2, v198
	ds_write_b32 v90, v95
	v_cndmask_b32_e64 v90, v196, v199, s[2:3]
	v_lshl_or_b32 v90, v90, 2, v198
	ds_write_b32 v90, v96
	v_cndmask_b32_e32 v90, v196, v199, vcc
	v_lshl_or_b32 v90, v90, 2, v198
	v_mfma_f32_16x16x32_bf16 v[138:141], v[18:21], v[132:135], v[136:139]
	ds_write_b32 v90, v97
	ds_read_b128 v[154:157], v197 offset:4608
	ds_read_b128 v[158:161], v197 offset:4672
	ds_read_b128 v[162:165], v197 offset:4736
	ds_read_b128 v[166:169], v197 offset:4800
	s_mov_b32 s18, 0x5dc000
	s_mov_b32 s19, 0x659000
	buffer_load_dwordx4 v[90:93], v201, s[8:11], s18 offen nt
	buffer_load_dwordx4 v[94:97], v201, s[8:11], s19 offen nt
	s_mov_b32 s18, 0x6d6000
	s_mov_b32 s19, 0x753000
	buffer_load_dwordx4 v[130:133], v201, s[8:11], s18 offen nt
	buffer_load_dwordx4 v[134:137], v201, s[8:11], s19 offen nt
	ds_write_b128 v200, v[58:61]
	s_waitcnt vmcnt(18)
	ds_write_b128 v200, v[62:65] offset:1152
	s_waitcnt vmcnt(17)
	ds_write_b128 v200, v[98:101] offset:2304
	s_waitcnt vmcnt(16)
	ds_write_b128 v200, v[102:105] offset:3456
	s_waitcnt lgkmcnt(7)
	v_cvt_pk_bf16_f32 v58, v154, v155
	v_cvt_pk_bf16_f32 v59, v156, v157
	s_waitcnt lgkmcnt(6)
	v_cvt_pk_bf16_f32 v60, v158, v159
	v_cvt_pk_bf16_f32 v61, v160, v161
	v_lshlrev_b32_e32 v98, 16, v58
	v_and_b32_e32 v99, 0xffff0000, v58
	v_mfma_f32_16x16x32_bf16 v[62:65], v[6:9], v[58:61], v[138:141]
	v_lshlrev_b32_e32 v100, 16, v59
	v_and_b32_e32 v101, 0xffff0000, v59
	v_pk_add_f32 v[98:99], v[154:155], v[98:99] neg_lo:[0,1] neg_hi:[0,1]
	v_mfma_f32_16x16x32_bf16 v[102:105], v[50:53], v[58:61], v[142:145]
	v_add_f32_e64 v100, v156, -v100
	v_add_f32_e64 v101, v157, -v101
	v_cvt_pk_bf16_f32 v98, v98, v99
	v_cvt_pk_bf16_f32 v99, v100, v101
	v_mfma_f32_16x16x32_bf16 v[62:65], v[14:17], v[58:61], v[62:65]
	v_lshlrev_b32_e32 v100, 16, v60
	v_and_b32_e32 v101, 0xffff0000, v60
	v_lshlrev_b32_e32 v142, 16, v61
	v_and_b32_e32 v143, 0xffff0000, v61
	v_pk_add_f32 v[100:101], v[158:159], v[100:101] neg_lo:[0,1] neg_hi:[0,1]
	v_mfma_f32_16x16x32_bf16 v[102:105], v[54:57], v[58:61], v[102:105]
	v_add_f32_e64 v142, v160, -v142
	v_add_f32_e64 v143, v161, -v143
	v_cvt_pk_bf16_f32 v100, v100, v101
	v_cvt_pk_bf16_f32 v101, v142, v143
	s_waitcnt lgkmcnt(5)
	v_cvt_pk_bf16_f32 v142, v162, v163
	v_mfma_f32_16x16x32_bf16 v[138:141], v[58:61], v[58:61], 0
	v_lshlrev_b32_e32 v144, 16, v142
	v_and_b32_e32 v145, 0xffff0000, v142
	v_cvt_pk_bf16_f32 v143, v164, v165
	v_mfma_f32_16x16x32_bf16 v[62:65], v[6:9], v[98:101], v[62:65]
	v_mfma_f32_16x16x32_bf16 v[58:61], v[58:61], v[98:101], 0
	v_mfma_f32_16x16x32_bf16 v[98:101], v[50:53], v[98:101], v[102:105]
	s_nop 2
	v_add_f32_e64 v102, v162, -v144
	v_add_f32_e64 v103, v163, -v145
	s_waitcnt lgkmcnt(4)
	v_cvt_pk_bf16_f32 v144, v166, v167
	v_cvt_pk_bf16_f32 v145, v168, v169
	v_lshlrev_b32_e32 v104, 16, v143
	v_and_b32_e32 v105, 0xffff0000, v143
	v_mfma_f32_16x16x32_bf16 v[62:65], v[2:5], v[142:145], v[62:65]
	v_add_f32_e64 v104, v164, -v104
	v_add_f32_e64 v105, v165, -v105
	v_cvt_pk_bf16_f32 v102, v102, v103
	v_cvt_pk_bf16_f32 v103, v104, v105
	v_lshlrev_b32_e32 v104, 16, v144
	v_and_b32_e32 v105, 0xffff0000, v144
	v_lshlrev_b32_e32 v154, 16, v145
	v_and_b32_e32 v155, 0xffff0000, v145
	v_mfma_f32_16x16x32_bf16 v[98:101], v[42:45], v[142:145], v[98:101]
	v_add_f32_e64 v104, v166, -v104
	v_add_f32_e64 v105, v167, -v105
	v_pk_add_f32 v[154:155], v[168:169], v[154:155] neg_lo:[0,1] neg_hi:[0,1]
	v_cvt_pk_bf16_f32 v104, v104, v105
	v_cvt_pk_bf16_f32 v105, v154, v155
	v_mfma_f32_16x16x32_bf16 v[138:141], v[142:145], v[142:145], v[138:141]
	v_mfma_f32_16x16x32_bf16 v[62:65], v[10:13], v[142:145], v[62:65]
	v_mfma_f32_16x16x32_bf16 v[58:61], v[142:145], v[102:105], v[58:61]
	v_mfma_f32_16x16x32_bf16 v[98:101], v[46:49], v[142:145], v[98:101]
	v_or_b32_e32 v142, 0x80, v199
	v_cndmask_b32_e64 v143, v196, v142, s[6:7]
	s_nop 4
	v_pk_fma_f32 v[140:141], v[60:61], 2.0, v[140:141] op_sel_hi:[1,0,1]
	v_pk_fma_f32 v[138:139], v[58:59], 2.0, v[138:139] op_sel_hi:[1,0,1]
	v_mfma_f32_16x16x32_bf16 v[58:61], v[2:5], v[102:105], v[62:65]
	s_nop 2
	v_lshl_or_b32 v62, v143, 2, v198
	ds_write_b32 v62, v138
	v_cndmask_b32_e64 v138, v196, v142, s[4:5]
	v_mfma_f32_16x16x32_bf16 v[62:65], v[42:45], v[102:105], v[98:101]
	s_nop 2
	v_lshl_or_b32 v98, v138, 2, v198
	ds_write_b32 v98, v139
	v_cndmask_b32_e64 v98, v196, v142, s[2:3]
	v_lshl_or_b32 v98, v98, 2, v198
	ds_write_b32 v98, v140
	v_cndmask_b32_e32 v98, v196, v142, vcc
	v_lshl_or_b32 v98, v98, 2, v198
	ds_write_b32 v98, v141
	ds_read_b128 v[154:157], v197
	ds_read_b128 v[158:161], v197 offset:64
	ds_read_b128 v[162:165], v197 offset:128
	ds_read_b128 v[166:169], v197 offset:192
	s_mov_b32 s18, 0x5dc100
	s_mov_b32 s19, 0x659100
	buffer_load_dwordx4 v[98:101], v201, s[8:11], s18 offen nt
	buffer_load_dwordx4 v[102:105], v201, s[8:11], s19 offen nt
	s_mov_b32 s18, 0x6d6100
	s_mov_b32 s19, 0x753100
	buffer_load_dwordx4 v[138:141], v201, s[8:11], s18 offen nt
	buffer_load_dwordx4 v[142:145], v201, s[8:11], s19 offen nt
	s_waitcnt vmcnt(19)
	ds_write_b128 v200, v[106:109] offset:4608
	s_waitcnt vmcnt(18)
	ds_write_b128 v200, v[110:113] offset:5760
	s_waitcnt vmcnt(17)
	ds_write_b128 v200, v[146:149] offset:6912
	s_waitcnt vmcnt(16)
	ds_write_b128 v200, v[150:153] offset:8064
	s_waitcnt lgkmcnt(7)
	v_cvt_pk_bf16_f32 v106, v154, v155
	v_cvt_pk_bf16_f32 v107, v156, v157
	s_waitcnt lgkmcnt(6)
	v_cvt_pk_bf16_f32 v108, v158, v159
	v_cvt_pk_bf16_f32 v109, v160, v161
	v_lshlrev_b32_e32 v146, 16, v106
	v_and_b32_e32 v147, 0xffff0000, v106
	v_mfma_f32_16x16x32_bf16 v[110:113], v[22:25], v[106:109], 0
	v_lshlrev_b32_e32 v148, 16, v107
	v_and_b32_e32 v149, 0xffff0000, v107
	v_pk_add_f32 v[146:147], v[154:155], v[146:147] neg_lo:[0,1] neg_hi:[0,1]
	v_mfma_f32_16x16x32_bf16 v[150:153], v[34:37], v[106:109], 0
	v_add_f32_e64 v148, v156, -v148
	v_add_f32_e64 v149, v157, -v149
	v_cvt_pk_bf16_f32 v146, v146, v147
	v_cvt_pk_bf16_f32 v147, v148, v149
	v_lshlrev_b32_e32 v148, 16, v108
	v_and_b32_e32 v149, 0xffff0000, v108
	v_mfma_f32_16x16x32_bf16 v[110:113], v[30:33], v[106:109], v[110:113]
	v_add_f32_e64 v148, v158, -v148
	v_add_f32_e64 v149, v159, -v149
	v_lshlrev_b32_e32 v158, 16, v109
	v_and_b32_e32 v159, 0xffff0000, v109
	v_pk_add_f32 v[158:159], v[160:161], v[158:159] neg_lo:[0,1] neg_hi:[0,1]
	v_cvt_pk_bf16_f32 v148, v148, v149
	v_mfma_f32_16x16x32_bf16 v[150:153], v[38:41], v[106:109], v[150:153]
	v_cvt_pk_bf16_f32 v149, v158, v159
	s_waitcnt lgkmcnt(5)
	v_cvt_pk_bf16_f32 v158, v162, v163
	v_lshlrev_b32_e32 v160, 16, v158
	v_mfma_f32_16x16x32_bf16 v[110:113], v[22:25], v[146:149], v[110:113]
	v_and_b32_e32 v161, 0xffff0000, v158
	v_cvt_pk_bf16_f32 v159, v164, v165
	v_mfma_f32_16x16x32_bf16 v[154:157], v[106:109], v[106:109], 0
	v_mfma_f32_16x16x32_bf16 v[106:109], v[106:109], v[146:149], 0
	v_mfma_f32_16x16x32_bf16 v[146:149], v[34:37], v[146:149], v[150:153]
	s_nop 2
	v_add_f32_e64 v150, v162, -v160
	v_add_f32_e64 v151, v163, -v161
	s_waitcnt lgkmcnt(4)
	v_cvt_pk_bf16_f32 v160, v166, v167
	v_cvt_pk_bf16_f32 v161, v168, v169
	v_lshlrev_b32_e32 v152, 16, v159
	v_and_b32_e32 v153, 0xffff0000, v159
	v_mfma_f32_16x16x32_bf16 v[110:113], v[18:21], v[158:161], v[110:113]
	v_add_f32_e64 v152, v164, -v152
	v_add_f32_e64 v153, v165, -v153
	v_cvt_pk_bf16_f32 v150, v150, v151
	v_cvt_pk_bf16_f32 v151, v152, v153
	v_lshlrev_b32_e32 v152, 16, v160
	v_and_b32_e32 v153, 0xffff0000, v160
	v_lshlrev_b32_e32 v162, 16, v161
	v_and_b32_e32 v163, 0xffff0000, v161
	v_pk_add_f32 v[152:153], v[166:167], v[152:153] neg_lo:[0,1] neg_hi:[0,1]
	v_pk_add_f32 v[162:163], v[168:169], v[162:163] neg_lo:[0,1] neg_hi:[0,1]
	v_mfma_f32_16x16x32_bf16 v[146:149], v[66:69], v[158:161], v[146:149]
	v_cvt_pk_bf16_f32 v152, v152, v153
	v_cvt_pk_bf16_f32 v153, v162, v163
	v_or_b32_e32 v162, 16, v199
	v_mfma_f32_16x16x32_bf16 v[154:157], v[158:161], v[158:161], v[154:157]
	v_mfma_f32_16x16x32_bf16 v[110:113], v[26:29], v[158:161], v[110:113]
	v_mfma_f32_16x16x32_bf16 v[106:109], v[158:161], v[150:153], v[106:109]
	v_mfma_f32_16x16x32_bf16 v[146:149], v[70:73], v[158:161], v[146:149]
	v_cndmask_b32_e64 v158, v196, v162, s[6:7]
	s_nop 5
	v_pk_fma_f32 v[108:109], v[108:109], 2.0, v[156:157] op_sel_hi:[1,0,1]
	v_pk_fma_f32 v[106:107], v[106:107], 2.0, v[154:155] op_sel_hi:[1,0,1]
	v_mfma_f32_16x16x32_bf16 v[154:157], v[18:21], v[150:153], v[110:113]
	s_nop 2
	v_lshl_or_b32 v110, v158, 2, v198
	ds_write_b32 v110, v106
	v_cndmask_b32_e64 v106, v196, v162, s[4:5]
	v_lshl_or_b32 v106, v106, 2, v198
	ds_write_b32 v106, v107
	v_cndmask_b32_e64 v106, v196, v162, s[2:3]
	v_lshl_or_b32 v106, v106, 2, v198
	ds_write_b32 v106, v108
	v_cndmask_b32_e32 v106, v196, v162, vcc
	v_lshl_or_b32 v106, v106, 2, v198
	v_mfma_f32_16x16x32_bf16 v[158:161], v[66:69], v[150:153], v[146:149]
	ds_write_b32 v106, v109
	ds_read_b128 v[162:165], v197 offset:4608
	ds_read_b128 v[166:169], v197 offset:4672
	ds_read_b128 v[170:173], v197 offset:4736
	ds_read_b128 v[174:177], v197 offset:4800
	s_mov_b32 s18, 0x7d0000
	s_mov_b32 s19, 0x84d000
	buffer_load_dwordx4 v[106:109], v201, s[8:11], s18 offen nt
	buffer_load_dwordx4 v[110:113], v201, s[8:11], s19 offen nt
	s_mov_b32 s18, 0x8ca000
	s_mov_b32 s19, 0x947000
	buffer_load_dwordx4 v[146:149], v201, s[8:11], s18 offen nt
	buffer_load_dwordx4 v[150:153], v201, s[8:11], s19 offen nt
	s_waitcnt vmcnt(19)
	ds_write_b128 v200, v[74:77]
	s_waitcnt vmcnt(18)
	ds_write_b128 v200, v[78:81] offset:1152
	s_waitcnt vmcnt(17)
	ds_write_b128 v200, v[114:117] offset:2304
	s_waitcnt vmcnt(16)
	ds_write_b128 v200, v[118:121] offset:3456
	s_waitcnt lgkmcnt(7)
	v_cvt_pk_bf16_f32 v74, v162, v163
	v_cvt_pk_bf16_f32 v75, v164, v165
	s_waitcnt lgkmcnt(6)
	v_cvt_pk_bf16_f32 v76, v166, v167
	v_cvt_pk_bf16_f32 v77, v168, v169
	v_lshlrev_b32_e32 v114, 16, v74
	v_and_b32_e32 v115, 0xffff0000, v74
	v_mfma_f32_16x16x32_bf16 v[78:81], v[6:9], v[74:77], v[154:157]
	v_lshlrev_b32_e32 v116, 16, v75
	v_and_b32_e32 v117, 0xffff0000, v75
	v_pk_add_f32 v[114:115], v[162:163], v[114:115] neg_lo:[0,1] neg_hi:[0,1]
	v_mfma_f32_16x16x32_bf16 v[118:121], v[50:53], v[74:77], v[158:161]
	v_add_f32_e64 v116, v164, -v116
	v_add_f32_e64 v117, v165, -v117
	v_cvt_pk_bf16_f32 v114, v114, v115
	v_cvt_pk_bf16_f32 v115, v116, v117
	v_mfma_f32_16x16x32_bf16 v[78:81], v[14:17], v[74:77], v[78:81]
	v_lshlrev_b32_e32 v116, 16, v76
	v_and_b32_e32 v117, 0xffff0000, v76
	v_lshlrev_b32_e32 v158, 16, v77
	v_and_b32_e32 v159, 0xffff0000, v77
	v_pk_add_f32 v[116:117], v[166:167], v[116:117] neg_lo:[0,1] neg_hi:[0,1]
	v_mfma_f32_16x16x32_bf16 v[118:121], v[54:57], v[74:77], v[118:121]
	v_add_f32_e64 v158, v168, -v158
	v_add_f32_e64 v159, v169, -v159
	v_cvt_pk_bf16_f32 v116, v116, v117
	v_cvt_pk_bf16_f32 v117, v158, v159
	s_waitcnt lgkmcnt(5)
	v_cvt_pk_bf16_f32 v158, v170, v171
	v_mfma_f32_16x16x32_bf16 v[154:157], v[74:77], v[74:77], 0
	v_lshlrev_b32_e32 v160, 16, v158
	v_and_b32_e32 v161, 0xffff0000, v158
	v_cvt_pk_bf16_f32 v159, v172, v173
	v_mfma_f32_16x16x32_bf16 v[78:81], v[6:9], v[114:117], v[78:81]
	v_mfma_f32_16x16x32_bf16 v[74:77], v[74:77], v[114:117], 0
	v_mfma_f32_16x16x32_bf16 v[114:117], v[50:53], v[114:117], v[118:121]
	s_nop 2
	v_add_f32_e64 v118, v170, -v160
	v_add_f32_e64 v119, v171, -v161
	s_waitcnt lgkmcnt(4)
	v_cvt_pk_bf16_f32 v160, v174, v175
	v_cvt_pk_bf16_f32 v161, v176, v177
	v_lshlrev_b32_e32 v120, 16, v159
	v_and_b32_e32 v121, 0xffff0000, v159
	v_mfma_f32_16x16x32_bf16 v[78:81], v[2:5], v[158:161], v[78:81]
	v_add_f32_e64 v120, v172, -v120
	v_add_f32_e64 v121, v173, -v121
	v_cvt_pk_bf16_f32 v118, v118, v119
	v_cvt_pk_bf16_f32 v119, v120, v121
	v_lshlrev_b32_e32 v120, 16, v160
	v_and_b32_e32 v121, 0xffff0000, v160
	v_lshlrev_b32_e32 v162, 16, v161
	v_and_b32_e32 v163, 0xffff0000, v161
	v_mfma_f32_16x16x32_bf16 v[114:117], v[42:45], v[158:161], v[114:117]
	v_add_f32_e64 v120, v174, -v120
	v_add_f32_e64 v121, v175, -v121
	v_pk_add_f32 v[162:163], v[176:177], v[162:163] neg_lo:[0,1] neg_hi:[0,1]
	v_cvt_pk_bf16_f32 v120, v120, v121
	v_cvt_pk_bf16_f32 v121, v162, v163
	v_mfma_f32_16x16x32_bf16 v[154:157], v[158:161], v[158:161], v[154:157]
	v_mfma_f32_16x16x32_bf16 v[78:81], v[10:13], v[158:161], v[78:81]
	v_mfma_f32_16x16x32_bf16 v[74:77], v[158:161], v[118:121], v[74:77]
	v_mfma_f32_16x16x32_bf16 v[114:117], v[46:49], v[158:161], v[114:117]
	v_or_b32_e32 v158, 0x90, v199
	v_cndmask_b32_e64 v159, v196, v158, s[6:7]
	s_nop 4
	v_pk_fma_f32 v[156:157], v[76:77], 2.0, v[156:157] op_sel_hi:[1,0,1]
	v_pk_fma_f32 v[154:155], v[74:75], 2.0, v[154:155] op_sel_hi:[1,0,1]
	v_mfma_f32_16x16x32_bf16 v[74:77], v[2:5], v[118:121], v[78:81]
	s_nop 2
	v_lshl_or_b32 v78, v159, 2, v198
	ds_write_b32 v78, v154
	v_cndmask_b32_e64 v154, v196, v158, s[4:5]
	v_mfma_f32_16x16x32_bf16 v[78:81], v[42:45], v[118:121], v[114:117]
	s_nop 2
	v_lshl_or_b32 v114, v154, 2, v198
	ds_write_b32 v114, v155
	v_cndmask_b32_e64 v114, v196, v158, s[2:3]
	v_lshl_or_b32 v114, v114, 2, v198
	ds_write_b32 v114, v156
	v_cndmask_b32_e32 v114, v196, v158, vcc
	v_lshl_or_b32 v114, v114, 2, v198
	ds_write_b32 v114, v157
	ds_read_b128 v[162:165], v197
	ds_read_b128 v[166:169], v197 offset:64
	ds_read_b128 v[170:173], v197 offset:128
	ds_read_b128 v[174:177], v197 offset:192
	s_mov_b32 s18, 0x7d0100
	s_mov_b32 s19, 0x84d100
	buffer_load_dwordx4 v[114:117], v201, s[8:11], s18 offen nt
	buffer_load_dwordx4 v[118:121], v201, s[8:11], s19 offen nt
	s_mov_b32 s18, 0x8ca100
	s_mov_b32 s19, 0x947100
	buffer_load_dwordx4 v[154:157], v201, s[8:11], s18 offen nt
	buffer_load_dwordx4 v[158:161], v201, s[8:11], s19 offen nt
	s_waitcnt vmcnt(19)
	ds_write_b128 v200, v[82:85] offset:4608
	s_waitcnt vmcnt(18)
	ds_write_b128 v200, v[86:89] offset:5760
	s_waitcnt vmcnt(17)
	ds_write_b128 v200, v[122:125] offset:6912
	s_waitcnt vmcnt(16)
	ds_write_b128 v200, v[126:129] offset:8064
	s_waitcnt lgkmcnt(7)
	v_cvt_pk_bf16_f32 v82, v162, v163
	v_cvt_pk_bf16_f32 v83, v164, v165
	s_waitcnt lgkmcnt(6)
	v_cvt_pk_bf16_f32 v84, v166, v167
	v_cvt_pk_bf16_f32 v85, v168, v169
	v_lshlrev_b32_e32 v122, 16, v82
	v_and_b32_e32 v123, 0xffff0000, v82
	v_mfma_f32_16x16x32_bf16 v[86:89], v[22:25], v[82:85], 0
	v_lshlrev_b32_e32 v124, 16, v83
	v_and_b32_e32 v125, 0xffff0000, v83
	v_pk_add_f32 v[122:123], v[162:163], v[122:123] neg_lo:[0,1] neg_hi:[0,1]
	v_mfma_f32_16x16x32_bf16 v[126:129], v[34:37], v[82:85], 0
	v_add_f32_e64 v124, v164, -v124
	v_add_f32_e64 v125, v165, -v125
	v_cvt_pk_bf16_f32 v122, v122, v123
	v_cvt_pk_bf16_f32 v123, v124, v125
	v_lshlrev_b32_e32 v124, 16, v84
	v_and_b32_e32 v125, 0xffff0000, v84
	v_mfma_f32_16x16x32_bf16 v[86:89], v[30:33], v[82:85], v[86:89]
	v_add_f32_e64 v124, v166, -v124
	v_add_f32_e64 v125, v167, -v125
	v_lshlrev_b32_e32 v166, 16, v85
	v_and_b32_e32 v167, 0xffff0000, v85
	v_mfma_f32_16x16x32_bf16 v[126:129], v[38:41], v[82:85], v[126:129]
	v_add_f32_e64 v166, v168, -v166
	v_add_f32_e64 v167, v169, -v167
	v_cvt_pk_bf16_f32 v124, v124, v125
	v_cvt_pk_bf16_f32 v125, v166, v167
	s_waitcnt lgkmcnt(5)
	v_cvt_pk_bf16_f32 v166, v170, v171
	v_mfma_f32_16x16x32_bf16 v[162:165], v[82:85], v[82:85], 0
	v_lshlrev_b32_e32 v168, 16, v166
	v_and_b32_e32 v169, 0xffff0000, v166
	v_cvt_pk_bf16_f32 v167, v172, v173
	v_mfma_f32_16x16x32_bf16 v[86:89], v[22:25], v[122:125], v[86:89]
	v_mfma_f32_16x16x32_bf16 v[82:85], v[82:85], v[122:125], 0
	v_mfma_f32_16x16x32_bf16 v[122:125], v[34:37], v[122:125], v[126:129]
	s_nop 2
	v_add_f32_e64 v126, v170, -v168
	v_add_f32_e64 v127, v171, -v169
	s_waitcnt lgkmcnt(4)
	v_cvt_pk_bf16_f32 v168, v174, v175
	v_cvt_pk_bf16_f32 v169, v176, v177
	v_lshlrev_b32_e32 v128, 16, v167
	v_and_b32_e32 v129, 0xffff0000, v167
	v_mfma_f32_16x16x32_bf16 v[86:89], v[18:21], v[166:169], v[86:89]
	v_add_f32_e64 v128, v172, -v128
	v_add_f32_e64 v129, v173, -v129
	v_cvt_pk_bf16_f32 v126, v126, v127
	v_cvt_pk_bf16_f32 v127, v128, v129
	v_lshlrev_b32_e32 v128, 16, v168
	v_and_b32_e32 v129, 0xffff0000, v168
	v_lshlrev_b32_e32 v170, 16, v169
	v_and_b32_e32 v171, 0xffff0000, v169
	v_mfma_f32_16x16x32_bf16 v[122:125], v[66:69], v[166:169], v[122:125]
	v_add_f32_e64 v128, v174, -v128
	v_add_f32_e64 v129, v175, -v129
	v_pk_add_f32 v[170:171], v[176:177], v[170:171] neg_lo:[0,1] neg_hi:[0,1]
	v_cvt_pk_bf16_f32 v128, v128, v129
	v_cvt_pk_bf16_f32 v129, v170, v171
	v_mfma_f32_16x16x32_bf16 v[162:165], v[166:169], v[166:169], v[162:165]
	v_mfma_f32_16x16x32_bf16 v[86:89], v[26:29], v[166:169], v[86:89]
	v_mfma_f32_16x16x32_bf16 v[82:85], v[166:169], v[126:129], v[82:85]
	v_mfma_f32_16x16x32_bf16 v[122:125], v[70:73], v[166:169], v[122:125]
	v_or_b32_e32 v166, 32, v199
	v_cndmask_b32_e64 v167, v196, v166, s[6:7]
	s_nop 4
	v_pk_fma_f32 v[164:165], v[84:85], 2.0, v[164:165] op_sel_hi:[1,0,1]
	v_pk_fma_f32 v[162:163], v[82:83], 2.0, v[162:163] op_sel_hi:[1,0,1]
	v_mfma_f32_16x16x32_bf16 v[82:85], v[18:21], v[126:129], v[86:89]
	s_nop 2
	v_lshl_or_b32 v86, v167, 2, v198
	ds_write_b32 v86, v162
	v_cndmask_b32_e64 v162, v196, v166, s[4:5]
	v_mfma_f32_16x16x32_bf16 v[86:89], v[66:69], v[126:129], v[122:125]
	s_nop 2
	v_lshl_or_b32 v122, v162, 2, v198
	ds_write_b32 v122, v163
	v_cndmask_b32_e64 v122, v196, v166, s[2:3]
	v_lshl_or_b32 v122, v122, 2, v198
	ds_write_b32 v122, v164
	v_cndmask_b32_e32 v122, v196, v166, vcc
	v_lshl_or_b32 v122, v122, 2, v198
	ds_write_b32 v122, v165
	ds_read_b128 v[170:173], v197 offset:4608
	ds_read_b128 v[174:177], v197 offset:4672
	ds_read_b128 v[178:181], v197 offset:4736
	ds_read_b128 v[182:185], v197 offset:4800
	s_mov_b32 s18, 0x9c4000
	s_mov_b32 s19, 0xa41000
	buffer_load_dwordx4 v[122:125], v201, s[8:11], s18 offen nt
	buffer_load_dwordx4 v[126:129], v201, s[8:11], s19 offen nt
	s_mov_b32 s18, 0xabe000
	s_mov_b32 s19, 0xb3b000
	buffer_load_dwordx4 v[162:165], v201, s[8:11], s18 offen nt
	buffer_load_dwordx4 v[166:169], v201, s[8:11], s19 offen nt
	s_waitcnt vmcnt(19)
	ds_write_b128 v200, v[90:93]
	s_waitcnt vmcnt(18)
	ds_write_b128 v200, v[94:97] offset:1152
	s_waitcnt vmcnt(17)
	ds_write_b128 v200, v[130:133] offset:2304
	s_waitcnt vmcnt(16)
	ds_write_b128 v200, v[134:137] offset:3456
	s_waitcnt lgkmcnt(7)
	v_cvt_pk_bf16_f32 v90, v170, v171
	v_cvt_pk_bf16_f32 v91, v172, v173
	s_waitcnt lgkmcnt(6)
	v_cvt_pk_bf16_f32 v92, v174, v175
	v_cvt_pk_bf16_f32 v93, v176, v177
	v_lshlrev_b32_e32 v94, 16, v90
	v_and_b32_e32 v95, 0xffff0000, v90
	v_mfma_f32_16x16x32_bf16 v[82:85], v[6:9], v[90:93], v[82:85]
	v_lshlrev_b32_e32 v96, 16, v91
	v_and_b32_e32 v97, 0xffff0000, v91
	v_pk_add_f32 v[94:95], v[170:171], v[94:95] neg_lo:[0,1] neg_hi:[0,1]
	v_mfma_f32_16x16x32_bf16 v[86:89], v[50:53], v[90:93], v[86:89]
	v_add_f32_e64 v96, v172, -v96
	v_add_f32_e64 v97, v173, -v97
	v_cvt_pk_bf16_f32 v94, v94, v95
	v_cvt_pk_bf16_f32 v95, v96, v97
	v_lshlrev_b32_e32 v96, 16, v92
	v_and_b32_e32 v97, 0xffff0000, v92
	v_mfma_f32_16x16x32_bf16 v[82:85], v[14:17], v[90:93], v[82:85]
	v_lshlrev_b32_e32 v134, 16, v93
	v_and_b32_e32 v135, 0xffff0000, v93
	v_pk_add_f32 v[96:97], v[174:175], v[96:97] neg_lo:[0,1] neg_hi:[0,1]
	v_mfma_f32_16x16x32_bf16 v[86:89], v[54:57], v[90:93], v[86:89]
	v_add_f32_e64 v134, v176, -v134
	v_add_f32_e64 v135, v177, -v135
	v_cvt_pk_bf16_f32 v96, v96, v97
	v_cvt_pk_bf16_f32 v97, v134, v135
	s_waitcnt lgkmcnt(5)
	v_cvt_pk_bf16_f32 v134, v178, v179
	v_lshlrev_b32_e32 v136, 16, v134
	v_and_b32_e32 v137, 0xffff0000, v134
	v_cvt_pk_bf16_f32 v135, v180, v181
	v_mfma_f32_16x16x32_bf16 v[130:133], v[90:93], v[90:93], 0
	v_mfma_f32_16x16x32_bf16 v[90:93], v[90:93], v[94:97], 0
	v_mfma_f32_16x16x32_bf16 v[82:85], v[6:9], v[94:97], v[82:85]
	v_mfma_f32_16x16x32_bf16 v[86:89], v[50:53], v[94:97], v[86:89]
	v_add_f32_e64 v94, v178, -v136
	v_add_f32_e64 v95, v179, -v137
	s_waitcnt lgkmcnt(4)
	v_cvt_pk_bf16_f32 v136, v182, v183
	v_cvt_pk_bf16_f32 v137, v184, v185
	v_lshlrev_b32_e32 v96, 16, v135
	v_and_b32_e32 v97, 0xffff0000, v135
	v_pk_add_f32 v[96:97], v[180:181], v[96:97] neg_lo:[0,1] neg_hi:[0,1]
	v_cvt_pk_bf16_f32 v94, v94, v95
	v_cvt_pk_bf16_f32 v95, v96, v97
	v_lshlrev_b32_e32 v96, 16, v136
	v_and_b32_e32 v97, 0xffff0000, v136
	v_lshlrev_b32_e32 v170, 16, v137
	v_and_b32_e32 v171, 0xffff0000, v137
	v_pk_add_f32 v[96:97], v[182:183], v[96:97] neg_lo:[0,1] neg_hi:[0,1]
	v_pk_add_f32 v[170:171], v[184:185], v[170:171] neg_lo:[0,1] neg_hi:[0,1]
	v_cvt_pk_bf16_f32 v96, v96, v97
	v_cvt_pk_bf16_f32 v97, v170, v171
	v_mfma_f32_16x16x32_bf16 v[130:133], v[134:137], v[134:137], v[130:133]
	s_nop 0
	v_mfma_f32_16x16x32_bf16 v[90:93], v[134:137], v[94:97], v[90:93]
	v_mfma_f32_16x16x32_bf16 v[82:85], v[2:5], v[134:137], v[82:85]
	v_mfma_f32_16x16x32_bf16 v[86:89], v[42:45], v[134:137], v[86:89]
	s_nop 5
	v_fma_f32 v90, v90, 2.0, v130
	v_fma_f32 v91, v91, 2.0, v131
	v_or_b32_e32 v130, 0xa0, v199
	v_cndmask_b32_e64 v131, v196, v130, s[6:7]
	v_mfma_f32_16x16x32_bf16 v[82:85], v[10:13], v[134:137], v[82:85]
	v_lshl_or_b32 v131, v131, 2, v198
	ds_write_b32 v131, v90
	v_cndmask_b32_e64 v90, v196, v130, s[4:5]
	v_mfma_f32_16x16x32_bf16 v[86:89], v[46:49], v[134:137], v[86:89]
	v_lshl_or_b32 v90, v90, 2, v198
	ds_write_b32 v90, v91
	v_cndmask_b32_e64 v90, v196, v130, s[2:3]
	v_mfma_f32_16x16x32_bf16 v[82:85], v[2:5], v[94:97], v[82:85]
	v_fma_f32 v92, v92, 2.0, v132
	v_fma_f32 v93, v93, 2.0, v133
	v_lshl_or_b32 v90, v90, 2, v198
	ds_write_b32 v90, v92
	v_mfma_f32_16x16x32_bf16 v[86:89], v[42:45], v[94:97], v[86:89]
	v_cndmask_b32_e32 v90, v196, v130, vcc
	v_lshl_or_b32 v90, v90, 2, v198
	ds_write_b32 v90, v93
	ds_read_b128 v[90:93], v197
	ds_read_b128 v[94:97], v197 offset:64
	ds_read_b128 v[178:181], v197 offset:128
	ds_read_b128 v[182:185], v197 offset:192
	s_mov_b32 s18, 0x9c4100
	s_mov_b32 s19, 0xa41100
	buffer_load_dwordx4 v[130:133], v201, s[8:11], s18 offen nt
	buffer_load_dwordx4 v[134:137], v201, s[8:11], s19 offen nt
	s_mov_b32 s18, 0xabe100
	s_mov_b32 s19, 0xb3b100
	buffer_load_dwordx4 v[170:173], v201, s[8:11], s18 offen nt
	buffer_load_dwordx4 v[174:177], v201, s[8:11], s19 offen nt
	s_waitcnt vmcnt(19)
	ds_write_b128 v200, v[98:101] offset:4608
	s_waitcnt vmcnt(18)
	ds_write_b128 v200, v[102:105] offset:5760
	s_waitcnt vmcnt(17)
	ds_write_b128 v200, v[138:141] offset:6912
	s_waitcnt vmcnt(16)
	ds_write_b128 v200, v[142:145] offset:8064
	s_waitcnt lgkmcnt(7)
	v_cvt_pk_bf16_f32 v98, v90, v91
	v_cvt_pk_bf16_f32 v99, v92, v93
	s_waitcnt lgkmcnt(6)
	v_cvt_pk_bf16_f32 v100, v94, v95
	v_cvt_pk_bf16_f32 v101, v96, v97
	v_lshlrev_b32_e32 v138, 16, v98
	v_and_b32_e32 v139, 0xffff0000, v98
	v_mfma_f32_16x16x32_bf16 v[102:105], v[22:25], v[98:101], 0
	v_add_f32_e64 v90, v90, -v138
	v_add_f32_e64 v91, v91, -v139
	v_lshlrev_b32_e32 v142, 16, v99
	v_and_b32_e32 v143, 0xffff0000, v99
	v_mfma_f32_16x16x32_bf16 v[138:141], v[34:37], v[98:101], 0
	v_add_f32_e64 v92, v92, -v142
	v_add_f32_e64 v93, v93, -v143
	v_cvt_pk_bf16_f32 v90, v90, v91
	v_cvt_pk_bf16_f32 v91, v92, v93
	v_lshlrev_b32_e32 v92, 16, v100
	v_and_b32_e32 v93, 0xffff0000, v100
	v_mfma_f32_16x16x32_bf16 v[102:105], v[30:33], v[98:101], v[102:105]
	v_add_f32_e64 v92, v94, -v92
	v_add_f32_e64 v93, v95, -v93
	v_lshlrev_b32_e32 v94, 16, v101
	v_and_b32_e32 v95, 0xffff0000, v101
	v_mfma_f32_16x16x32_bf16 v[138:141], v[38:41], v[98:101], v[138:141]
	v_add_f32_e64 v94, v96, -v94
	v_add_f32_e64 v95, v97, -v95
	v_cvt_pk_bf16_f32 v92, v92, v93
	v_cvt_pk_bf16_f32 v93, v94, v95
	v_mfma_f32_16x16x32_bf16 v[142:145], v[98:101], v[98:101], 0
	s_nop 0
	v_mfma_f32_16x16x32_bf16 v[94:97], v[98:101], v[90:93], 0
	v_mfma_f32_16x16x32_bf16 v[98:101], v[22:25], v[90:93], v[102:105]
	s_waitcnt lgkmcnt(5)
	s_nop 1
	v_cvt_pk_bf16_f32 v102, v178, v179
	v_lshlrev_b32_e32 v104, 16, v102
	v_and_b32_e32 v105, 0xffff0000, v102
	v_mfma_f32_16x16x32_bf16 v[90:93], v[34:37], v[90:93], v[138:141]
	v_add_f32_e64 v104, v178, -v104
	v_add_f32_e64 v105, v179, -v105
	v_cvt_pk_bf16_f32 v103, v180, v181
	v_cvt_pk_bf16_f32 v138, v104, v105
	s_waitcnt lgkmcnt(4)
	v_cvt_pk_bf16_f32 v104, v182, v183
	v_cvt_pk_bf16_f32 v105, v184, v185
	v_lshlrev_b32_e32 v140, 16, v103
	v_and_b32_e32 v141, 0xffff0000, v103
	v_mfma_f32_16x16x32_bf16 v[98:101], v[18:21], v[102:105], v[98:101]
	v_add_f32_e64 v140, v180, -v140
	v_add_f32_e64 v141, v181, -v141
	v_lshlrev_b32_e32 v178, 16, v105
	v_cvt_pk_bf16_f32 v139, v140, v141
	v_lshlrev_b32_e32 v140, 16, v104
	v_and_b32_e32 v141, 0xffff0000, v104
	v_and_b32_e32 v179, 0xffff0000, v105
	v_mfma_f32_16x16x32_bf16 v[90:93], v[66:69], v[102:105], v[90:93]
	v_add_f32_e64 v140, v182, -v140
	v_add_f32_e64 v141, v183, -v141
	v_pk_add_f32 v[178:179], v[184:185], v[178:179] neg_lo:[0,1] neg_hi:[0,1]
	v_cvt_pk_bf16_f32 v140, v140, v141
	v_cvt_pk_bf16_f32 v141, v178, v179
	v_mfma_f32_16x16x32_bf16 v[142:145], v[102:105], v[102:105], v[142:145]
	v_mfma_f32_16x16x32_bf16 v[98:101], v[26:29], v[102:105], v[98:101]
	v_mfma_f32_16x16x32_bf16 v[94:97], v[102:105], v[138:141], v[94:97]
	v_mfma_f32_16x16x32_bf16 v[90:93], v[70:73], v[102:105], v[90:93]
	v_or_b32_e32 v104, 48, v199
	v_cndmask_b32_e64 v105, v196, v104, s[6:7]
	s_nop 4
	v_pk_fma_f32 v[144:145], v[96:97], 2.0, v[144:145] op_sel_hi:[1,0,1]
	v_pk_fma_f32 v[102:103], v[94:95], 2.0, v[142:143] op_sel_hi:[1,0,1]
	v_mfma_f32_16x16x32_bf16 v[94:97], v[18:21], v[138:141], v[98:101]
	s_nop 2
	v_lshl_or_b32 v98, v105, 2, v198
	ds_write_b32 v98, v102
	v_cndmask_b32_e64 v98, v196, v104, s[4:5]
	v_lshl_or_b32 v98, v98, 2, v198
	v_mfma_f32_16x16x32_bf16 v[90:93], v[66:69], v[138:141], v[90:93]
	ds_write_b32 v98, v103
	v_cndmask_b32_e64 v98, v196, v104, s[2:3]
	v_lshl_or_b32 v98, v98, 2, v198
	ds_write_b32 v98, v144
	v_cndmask_b32_e32 v98, v196, v104, vcc
	v_lshl_or_b32 v98, v98, 2, v198
	ds_write_b32 v98, v145
	ds_read_b128 v[98:101], v197 offset:4608
	ds_read_b128 v[102:105], v197 offset:4672
	ds_read_b128 v[186:189], v197 offset:4736
	ds_read_b128 v[190:193], v197 offset:4800
	s_mov_b32 s18, 0xbb8000
	s_mov_b32 s19, 0xc35000
	buffer_load_dwordx4 v[138:141], v201, s[8:11], s18 offen nt
	buffer_load_dwordx4 v[142:145], v201, s[8:11], s19 offen nt
	s_mov_b32 s18, 0xcb2000
	s_mov_b32 s19, 0xd2f000
	buffer_load_dwordx4 v[178:181], v201, s[8:11], s18 offen nt
	buffer_load_dwordx4 v[182:185], v201, s[8:11], s19 offen nt
	s_waitcnt vmcnt(19)
	ds_write_b128 v200, v[106:109]
	s_waitcnt vmcnt(18)
	ds_write_b128 v200, v[110:113] offset:1152
	s_waitcnt vmcnt(17)
	ds_write_b128 v200, v[146:149] offset:2304
	s_waitcnt vmcnt(16)
	ds_write_b128 v200, v[150:153] offset:3456
	s_waitcnt lgkmcnt(7)
	v_cvt_pk_bf16_f32 v106, v98, v99
	v_cvt_pk_bf16_f32 v107, v100, v101
	s_waitcnt lgkmcnt(6)
	v_cvt_pk_bf16_f32 v108, v102, v103
	v_cvt_pk_bf16_f32 v109, v104, v105
	v_lshlrev_b32_e32 v110, 16, v106
	v_and_b32_e32 v111, 0xffff0000, v106
	v_mfma_f32_16x16x32_bf16 v[94:97], v[6:9], v[106:109], v[94:97]
	v_add_f32_e64 v98, v98, -v110
	v_add_f32_e64 v99, v99, -v111
	v_lshlrev_b32_e32 v110, 16, v107
	v_and_b32_e32 v111, 0xffff0000, v107
	v_mfma_f32_16x16x32_bf16 v[90:93], v[50:53], v[106:109], v[90:93]
	v_add_f32_e64 v100, v100, -v110
	v_add_f32_e64 v101, v101, -v111
	v_cvt_pk_bf16_f32 v98, v98, v99
	v_cvt_pk_bf16_f32 v99, v100, v101
	v_lshlrev_b32_e32 v100, 16, v108
	v_and_b32_e32 v101, 0xffff0000, v108
	v_mfma_f32_16x16x32_bf16 v[94:97], v[14:17], v[106:109], v[94:97]
	v_add_f32_e64 v100, v102, -v100
	v_add_f32_e64 v101, v103, -v101
	v_lshlrev_b32_e32 v102, 16, v109
	v_and_b32_e32 v103, 0xffff0000, v109
	v_mfma_f32_16x16x32_bf16 v[90:93], v[54:57], v[106:109], v[90:93]
	v_add_f32_e64 v102, v104, -v102
	v_add_f32_e64 v103, v105, -v103
	v_cvt_pk_bf16_f32 v100, v100, v101
	v_cvt_pk_bf16_f32 v101, v102, v103
	v_mfma_f32_16x16x32_bf16 v[110:113], v[106:109], v[106:109], 0
	s_nop 0
	v_mfma_f32_16x16x32_bf16 v[102:105], v[106:109], v[98:101], 0
	s_waitcnt lgkmcnt(5)
	v_cvt_pk_bf16_f32 v106, v186, v187
	v_lshlrev_b32_e32 v108, 16, v106
	v_and_b32_e32 v109, 0xffff0000, v106
	v_mfma_f32_16x16x32_bf16 v[94:97], v[6:9], v[98:101], v[94:97]
	v_cvt_pk_bf16_f32 v107, v188, v189
	v_mfma_f32_16x16x32_bf16 v[90:93], v[50:53], v[98:101], v[90:93]
	v_add_f32_e64 v98, v186, -v108
	v_add_f32_e64 v99, v187, -v109
	s_waitcnt lgkmcnt(4)
	v_cvt_pk_bf16_f32 v108, v190, v191
	v_cvt_pk_bf16_f32 v109, v192, v193
	v_lshlrev_b32_e32 v100, 16, v107
	v_and_b32_e32 v101, 0xffff0000, v107
	v_pk_add_f32 v[100:101], v[188:189], v[100:101] neg_lo:[0,1] neg_hi:[0,1]
	v_cvt_pk_bf16_f32 v98, v98, v99
	v_cvt_pk_bf16_f32 v99, v100, v101
	v_lshlrev_b32_e32 v100, 16, v108
	v_and_b32_e32 v101, 0xffff0000, v108
	v_lshlrev_b32_e32 v146, 16, v109
	v_and_b32_e32 v147, 0xffff0000, v109
	v_mfma_f32_16x16x32_bf16 v[94:97], v[2:5], v[106:109], v[94:97]
	v_add_f32_e64 v100, v190, -v100
	v_add_f32_e64 v101, v191, -v101
	v_pk_add_f32 v[146:147], v[192:193], v[146:147] neg_lo:[0,1] neg_hi:[0,1]
	v_cvt_pk_bf16_f32 v100, v100, v101
	v_cvt_pk_bf16_f32 v101, v146, v147
	v_mfma_f32_16x16x32_bf16 v[90:93], v[42:45], v[106:109], v[90:93]
	v_mfma_f32_16x16x32_bf16 v[110:113], v[106:109], v[106:109], v[110:113]
	v_mfma_f32_16x16x32_bf16 v[102:105], v[106:109], v[98:101], v[102:105]
	v_mfma_f32_16x16x32_bf16 v[94:97], v[10:13], v[106:109], v[94:97]
	s_nop 6
	v_fma_f32 v112, v104, 2.0, v112
	v_fma_f32 v113, v105, 2.0, v113
	v_mfma_f32_16x16x32_bf16 v[104:107], v[46:49], v[106:109], v[90:93]
	v_or_b32_e32 v108, 0xb0, v199
	v_cndmask_b32_e64 v109, v196, v108, s[6:7]
	v_pk_fma_f32 v[102:103], v[102:103], 2.0, v[110:111] op_sel_hi:[1,0,1]
	v_mfma_f32_16x16x32_bf16 v[90:93], v[2:5], v[98:101], v[94:97]
	s_nop 2
	v_lshl_or_b32 v94, v109, 2, v198
	ds_write_b32 v94, v102
	v_cndmask_b32_e64 v102, v196, v108, s[4:5]
	v_mfma_f32_16x16x32_bf16 v[94:97], v[42:45], v[98:101], v[104:107]
	v_lshl_or_b32 v98, v102, 2, v198
	ds_write_b32 v98, v103
	v_cndmask_b32_e64 v98, v196, v108, s[2:3]
	v_lshl_or_b32 v98, v98, 2, v198
	ds_write_b32 v98, v112
	v_cndmask_b32_e32 v98, v196, v108, vcc
	v_lshl_or_b32 v98, v98, 2, v198
	ds_write_b32 v98, v113
	ds_read_b128 v[98:101], v197
	ds_read_b128 v[102:105], v197 offset:64
	ds_read_b128 v[106:109], v197 offset:128
	ds_read_b128 v[110:113], v197 offset:192
	s_mov_b32 s18, 0xbb8100
	s_mov_b32 s19, 0xc35100
	buffer_load_dwordx4 v[146:149], v201, s[8:11], s18 offen nt
	buffer_load_dwordx4 v[150:153], v201, s[8:11], s19 offen nt
	s_mov_b32 s18, 0xcb2100
	s_mov_b32 s19, 0xd2f100
	buffer_load_dwordx4 v[186:189], v201, s[8:11], s18 offen nt
	buffer_load_dwordx4 v[190:193], v201, s[8:11], s19 offen nt
	s_waitcnt vmcnt(19)
	ds_write_b128 v200, v[114:117] offset:4608
	s_waitcnt vmcnt(18)
	ds_write_b128 v200, v[118:121] offset:5760
	s_waitcnt vmcnt(17)
	ds_write_b128 v200, v[154:157] offset:6912
	s_waitcnt vmcnt(16)
	ds_write_b128 v200, v[158:161] offset:8064
	s_waitcnt lgkmcnt(7)
	v_cvt_pk_bf16_f32 v114, v98, v99
	v_cvt_pk_bf16_f32 v115, v100, v101
	s_waitcnt lgkmcnt(6)
	v_cvt_pk_bf16_f32 v116, v102, v103
	v_cvt_pk_bf16_f32 v117, v104, v105
	v_lshlrev_b32_e32 v154, 16, v114
	v_and_b32_e32 v155, 0xffff0000, v114
	v_mfma_f32_16x16x32_bf16 v[118:121], v[22:25], v[114:117], 0
	v_add_f32_e64 v98, v98, -v154
	v_add_f32_e64 v99, v99, -v155
	v_lshlrev_b32_e32 v158, 16, v115
	v_and_b32_e32 v159, 0xffff0000, v115
	v_mfma_f32_16x16x32_bf16 v[154:157], v[34:37], v[114:117], 0
	v_add_f32_e64 v100, v100, -v158
	v_add_f32_e64 v101, v101, -v159
	v_cvt_pk_bf16_f32 v98, v98, v99
	v_cvt_pk_bf16_f32 v99, v100, v101
	v_lshlrev_b32_e32 v100, 16, v116
	v_and_b32_e32 v101, 0xffff0000, v116
	v_mfma_f32_16x16x32_bf16 v[118:121], v[30:33], v[114:117], v[118:121]
	v_add_f32_e64 v100, v102, -v100
	v_add_f32_e64 v101, v103, -v101
	v_lshlrev_b32_e32 v102, 16, v117
	v_and_b32_e32 v103, 0xffff0000, v117
	v_mfma_f32_16x16x32_bf16 v[154:157], v[38:41], v[114:117], v[154:157]
	v_add_f32_e64 v102, v104, -v102
	v_add_f32_e64 v103, v105, -v103
	v_cvt_pk_bf16_f32 v100, v100, v101
	v_cvt_pk_bf16_f32 v101, v102, v103
	v_mfma_f32_16x16x32_bf16 v[158:161], v[114:117], v[114:117], 0
	s_nop 0
	v_mfma_f32_16x16x32_bf16 v[102:105], v[114:117], v[98:101], 0
	v_mfma_f32_16x16x32_bf16 v[114:117], v[22:25], v[98:101], v[118:121]
	s_waitcnt lgkmcnt(5)
	s_nop 1
	v_cvt_pk_bf16_f32 v118, v106, v107
	v_cvt_pk_bf16_f32 v119, v108, v109
	v_lshlrev_b32_e32 v120, 16, v118
	v_and_b32_e32 v121, 0xffff0000, v118
	v_mfma_f32_16x16x32_bf16 v[98:101], v[34:37], v[98:101], v[154:157]
	v_add_f32_e64 v106, v106, -v120
	v_add_f32_e64 v107, v107, -v121
	s_waitcnt lgkmcnt(4)
	v_cvt_pk_bf16_f32 v120, v110, v111
	v_cvt_pk_bf16_f32 v121, v112, v113
	v_lshlrev_b32_e32 v154, 16, v119
	v_and_b32_e32 v155, 0xffff0000, v119
	v_pk_add_f32 v[108:109], v[108:109], v[154:155] neg_lo:[0,1] neg_hi:[0,1]
	v_cvt_pk_bf16_f32 v106, v106, v107
	v_mfma_f32_16x16x32_bf16 v[114:117], v[18:21], v[118:121], v[114:117]
	v_cvt_pk_bf16_f32 v107, v108, v109
	v_lshlrev_b32_e32 v108, 16, v120
	v_and_b32_e32 v109, 0xffff0000, v120
	v_pk_add_f32 v[108:109], v[110:111], v[108:109] neg_lo:[0,1] neg_hi:[0,1]
	v_lshlrev_b32_e32 v110, 16, v121
	v_and_b32_e32 v111, 0xffff0000, v121
	v_mfma_f32_16x16x32_bf16 v[98:101], v[66:69], v[118:121], v[98:101]
	v_add_f32_e64 v110, v112, -v110
	v_add_f32_e64 v111, v113, -v111
	v_cvt_pk_bf16_f32 v108, v108, v109
	v_cvt_pk_bf16_f32 v109, v110, v111
	v_mfma_f32_16x16x32_bf16 v[154:157], v[118:121], v[118:121], v[158:161]
	v_mfma_f32_16x16x32_bf16 v[114:117], v[26:29], v[118:121], v[114:117]
	v_mfma_f32_16x16x32_bf16 v[102:105], v[118:121], v[106:109], v[102:105]
	v_mfma_f32_16x16x32_bf16 v[98:101], v[70:73], v[118:121], v[98:101]
	v_or_b32_e32 v118, 64, v199
	v_cndmask_b32_e64 v119, v196, v118, s[6:7]
	s_nop 4
	v_pk_fma_f32 v[110:111], v[104:105], 2.0, v[156:157] op_sel_hi:[1,0,1]
	v_pk_fma_f32 v[112:113], v[102:103], 2.0, v[154:155] op_sel_hi:[1,0,1]
	v_mfma_f32_16x16x32_bf16 v[102:105], v[18:21], v[106:109], v[114:117]
	s_nop 2
	v_lshl_or_b32 v114, v119, 2, v198
	ds_write_b32 v114, v112
	v_cndmask_b32_e64 v112, v196, v118, s[4:5]
	v_mfma_f32_16x16x32_bf16 v[98:101], v[66:69], v[106:109], v[98:101]
	v_lshl_or_b32 v106, v112, 2, v198
	ds_write_b32 v106, v113
	v_cndmask_b32_e64 v106, v196, v118, s[2:3]
	v_lshl_or_b32 v106, v106, 2, v198
	ds_write_b32 v106, v110
	v_cndmask_b32_e32 v106, v196, v118, vcc
	v_lshl_or_b32 v106, v106, 2, v198
	ds_write_b32 v106, v111
	ds_read_b128 v[106:109], v197 offset:4608
	ds_read_b128 v[110:113], v197 offset:4672
	ds_read_b128 v[202:205], v197 offset:4736
	ds_read_b128 v[206:209], v197 offset:4800
	s_mov_b32 s18, 0xdac000
	s_mov_b32 s19, 0xe29000
	buffer_load_dwordx4 v[114:117], v201, s[8:11], s18 offen nt
	buffer_load_dwordx4 v[118:121], v201, s[8:11], s19 offen nt
	s_mov_b32 s18, 0xea6000
	s_mov_b32 s19, 0xf23000
	buffer_load_dwordx4 v[154:157], v201, s[8:11], s18 offen nt
	buffer_load_dwordx4 v[158:161], v201, s[8:11], s19 offen nt
	s_waitcnt vmcnt(19)
	ds_write_b128 v200, v[122:125]
	s_waitcnt vmcnt(18)
	ds_write_b128 v200, v[126:129] offset:1152
	s_waitcnt vmcnt(17)
	ds_write_b128 v200, v[162:165] offset:2304
	s_waitcnt vmcnt(16)
	ds_write_b128 v200, v[166:169] offset:3456
	s_waitcnt lgkmcnt(7)
	v_cvt_pk_bf16_f32 v122, v106, v107
	v_cvt_pk_bf16_f32 v123, v108, v109
	s_waitcnt lgkmcnt(6)
	v_cvt_pk_bf16_f32 v124, v110, v111
	v_cvt_pk_bf16_f32 v125, v112, v113
	v_lshlrev_b32_e32 v126, 16, v122
	v_and_b32_e32 v127, 0xffff0000, v122
	v_mfma_f32_16x16x32_bf16 v[102:105], v[6:9], v[122:125], v[102:105]
	v_add_f32_e64 v106, v106, -v126
	v_add_f32_e64 v107, v107, -v127
	v_lshlrev_b32_e32 v126, 16, v123
	v_and_b32_e32 v127, 0xffff0000, v123
	v_mfma_f32_16x16x32_bf16 v[98:101], v[50:53], v[122:125], v[98:101]
	v_add_f32_e64 v108, v108, -v126
	v_add_f32_e64 v109, v109, -v127
	v_cvt_pk_bf16_f32 v106, v106, v107
	v_cvt_pk_bf16_f32 v107, v108, v109
	v_lshlrev_b32_e32 v108, 16, v124
	v_and_b32_e32 v109, 0xffff0000, v124
	v_mfma_f32_16x16x32_bf16 v[102:105], v[14:17], v[122:125], v[102:105]
	v_add_f32_e64 v108, v110, -v108
	v_add_f32_e64 v109, v111, -v109
	v_lshlrev_b32_e32 v110, 16, v125
	v_and_b32_e32 v111, 0xffff0000, v125
	v_mfma_f32_16x16x32_bf16 v[98:101], v[54:57], v[122:125], v[98:101]
	v_add_f32_e64 v110, v112, -v110
	v_add_f32_e64 v111, v113, -v111
	v_cvt_pk_bf16_f32 v108, v108, v109
	v_cvt_pk_bf16_f32 v109, v110, v111
	v_mfma_f32_16x16x32_bf16 v[126:129], v[122:125], v[122:125], 0
	s_nop 0
	v_mfma_f32_16x16x32_bf16 v[110:113], v[122:125], v[106:109], 0
	s_waitcnt lgkmcnt(5)
	v_cvt_pk_bf16_f32 v122, v202, v203
	v_lshlrev_b32_e32 v124, 16, v122
	v_and_b32_e32 v125, 0xffff0000, v122
	v_mfma_f32_16x16x32_bf16 v[102:105], v[6:9], v[106:109], v[102:105]
	v_cvt_pk_bf16_f32 v123, v204, v205
	v_mfma_f32_16x16x32_bf16 v[98:101], v[50:53], v[106:109], v[98:101]
	v_add_f32_e64 v106, v202, -v124
	v_add_f32_e64 v107, v203, -v125
	s_waitcnt lgkmcnt(4)
	v_cvt_pk_bf16_f32 v124, v206, v207
	v_cvt_pk_bf16_f32 v125, v208, v209
	v_lshlrev_b32_e32 v108, 16, v123
	v_and_b32_e32 v109, 0xffff0000, v123
	v_pk_add_f32 v[108:109], v[204:205], v[108:109] neg_lo:[0,1] neg_hi:[0,1]
	v_cvt_pk_bf16_f32 v106, v106, v107
	v_cvt_pk_bf16_f32 v107, v108, v109
	v_lshlrev_b32_e32 v108, 16, v124
	v_and_b32_e32 v109, 0xffff0000, v124
	v_lshlrev_b32_e32 v162, 16, v125
	v_and_b32_e32 v163, 0xffff0000, v125
	v_mfma_f32_16x16x32_bf16 v[102:105], v[2:5], v[122:125], v[102:105]
	v_add_f32_e64 v108, v206, -v108
	v_add_f32_e64 v109, v207, -v109
	v_pk_add_f32 v[162:163], v[208:209], v[162:163] neg_lo:[0,1] neg_hi:[0,1]
	v_cvt_pk_bf16_f32 v108, v108, v109
	v_cvt_pk_bf16_f32 v109, v162, v163
	v_mfma_f32_16x16x32_bf16 v[98:101], v[42:45], v[122:125], v[98:101]
	v_mfma_f32_16x16x32_bf16 v[126:129], v[122:125], v[122:125], v[126:129]
	v_mfma_f32_16x16x32_bf16 v[110:113], v[122:125], v[106:109], v[110:113]
	v_mfma_f32_16x16x32_bf16 v[102:105], v[10:13], v[122:125], v[102:105]
	v_mfma_f32_16x16x32_bf16 v[122:125], v[46:49], v[122:125], v[98:101]
	s_nop 5
	v_fma_f32 v110, v110, 2.0, v126
	v_fma_f32 v111, v111, 2.0, v127
	v_or_b32_e32 v126, 0xc0, v199
	v_cndmask_b32_e64 v127, v196, v126, s[6:7]
	v_mfma_f32_16x16x32_bf16 v[98:101], v[2:5], v[106:109], v[102:105]
	v_fma_f32 v112, v112, 2.0, v128
	v_fma_f32 v113, v113, 2.0, v129
	s_nop 0
	v_lshl_or_b32 v102, v127, 2, v198
	ds_write_b32 v102, v110
	v_cndmask_b32_e64 v110, v196, v126, s[4:5]
	v_mfma_f32_16x16x32_bf16 v[102:105], v[42:45], v[106:109], v[122:125]
	v_lshl_or_b32 v106, v110, 2, v198
	ds_write_b32 v106, v111
	v_cndmask_b32_e64 v106, v196, v126, s[2:3]
	v_lshl_or_b32 v106, v106, 2, v198
	ds_write_b32 v106, v112
	v_cndmask_b32_e32 v106, v196, v126, vcc
	v_lshl_or_b32 v106, v106, 2, v198
	ds_write_b32 v106, v113
	ds_read_b128 v[106:109], v197
	ds_read_b128 v[110:113], v197 offset:64
	ds_read_b128 v[202:205], v197 offset:128
	ds_read_b128 v[206:209], v197 offset:192
	s_mov_b32 s18, 0xdac100
	s_mov_b32 s19, 0xe29100
	buffer_load_dwordx4 v[122:125], v201, s[8:11], s18 offen nt
	buffer_load_dwordx4 v[126:129], v201, s[8:11], s19 offen nt
	s_mov_b32 s18, 0xea6100
	s_mov_b32 s19, 0xf23100
	buffer_load_dwordx4 v[162:165], v201, s[8:11], s18 offen nt
	buffer_load_dwordx4 v[166:169], v201, s[8:11], s19 offen nt
	s_waitcnt vmcnt(19)
	ds_write_b128 v200, v[130:133] offset:4608
	s_waitcnt vmcnt(18)
	ds_write_b128 v200, v[134:137] offset:5760
	s_waitcnt vmcnt(17)
	ds_write_b128 v200, v[170:173] offset:6912
	s_waitcnt vmcnt(16)
	ds_write_b128 v200, v[174:177] offset:8064
	s_waitcnt lgkmcnt(7)
	v_cvt_pk_bf16_f32 v130, v106, v107
	v_cvt_pk_bf16_f32 v131, v108, v109
	s_waitcnt lgkmcnt(6)
	v_cvt_pk_bf16_f32 v132, v110, v111
	v_cvt_pk_bf16_f32 v133, v112, v113
	v_lshlrev_b32_e32 v170, 16, v130
	v_and_b32_e32 v171, 0xffff0000, v130
	v_mfma_f32_16x16x32_bf16 v[134:137], v[22:25], v[130:133], 0
	v_add_f32_e64 v106, v106, -v170
	v_add_f32_e64 v107, v107, -v171
	v_lshlrev_b32_e32 v174, 16, v131
	v_and_b32_e32 v175, 0xffff0000, v131
	v_mfma_f32_16x16x32_bf16 v[170:173], v[34:37], v[130:133], 0
	v_add_f32_e64 v108, v108, -v174
	v_add_f32_e64 v109, v109, -v175
	v_cvt_pk_bf16_f32 v106, v106, v107
	v_cvt_pk_bf16_f32 v107, v108, v109
	v_lshlrev_b32_e32 v108, 16, v132
	v_and_b32_e32 v109, 0xffff0000, v132
	v_mfma_f32_16x16x32_bf16 v[134:137], v[30:33], v[130:133], v[134:137]
	v_add_f32_e64 v108, v110, -v108
	v_add_f32_e64 v109, v111, -v109
	v_lshlrev_b32_e32 v110, 16, v133
	v_and_b32_e32 v111, 0xffff0000, v133
	v_mfma_f32_16x16x32_bf16 v[170:173], v[38:41], v[130:133], v[170:173]
	v_add_f32_e64 v110, v112, -v110
	v_add_f32_e64 v111, v113, -v111
	v_cvt_pk_bf16_f32 v108, v108, v109
	v_cvt_pk_bf16_f32 v109, v110, v111
	v_mfma_f32_16x16x32_bf16 v[174:177], v[130:133], v[130:133], 0
	s_nop 0
	v_mfma_f32_16x16x32_bf16 v[110:113], v[130:133], v[106:109], 0
	v_mfma_f32_16x16x32_bf16 v[130:133], v[22:25], v[106:109], v[134:137]
	s_waitcnt lgkmcnt(5)
	s_nop 1
	v_cvt_pk_bf16_f32 v134, v202, v203
	v_lshlrev_b32_e32 v136, 16, v134
	v_and_b32_e32 v137, 0xffff0000, v134
	v_mfma_f32_16x16x32_bf16 v[106:109], v[34:37], v[106:109], v[170:173]
	v_add_f32_e64 v136, v202, -v136
	v_add_f32_e64 v137, v203, -v137
	v_cvt_pk_bf16_f32 v135, v204, v205
	v_cvt_pk_bf16_f32 v170, v136, v137
	s_waitcnt lgkmcnt(4)
	v_cvt_pk_bf16_f32 v136, v206, v207
	v_cvt_pk_bf16_f32 v137, v208, v209
	v_lshlrev_b32_e32 v172, 16, v135
	v_and_b32_e32 v173, 0xffff0000, v135
	v_mfma_f32_16x16x32_bf16 v[130:133], v[18:21], v[134:137], v[130:133]
	v_add_f32_e64 v172, v204, -v172
	v_add_f32_e64 v173, v205, -v173
	v_lshlrev_b32_e32 v202, 16, v137
	v_cvt_pk_bf16_f32 v171, v172, v173
	v_lshlrev_b32_e32 v172, 16, v136
	v_and_b32_e32 v173, 0xffff0000, v136
	v_and_b32_e32 v203, 0xffff0000, v137
	v_mfma_f32_16x16x32_bf16 v[106:109], v[66:69], v[134:137], v[106:109]
	v_add_f32_e64 v172, v206, -v172
	v_add_f32_e64 v173, v207, -v173
	v_pk_add_f32 v[202:203], v[208:209], v[202:203] neg_lo:[0,1] neg_hi:[0,1]
	v_cvt_pk_bf16_f32 v172, v172, v173
	v_cvt_pk_bf16_f32 v173, v202, v203
	v_mfma_f32_16x16x32_bf16 v[174:177], v[134:137], v[134:137], v[174:177]
	v_mfma_f32_16x16x32_bf16 v[130:133], v[26:29], v[134:137], v[130:133]
	v_mfma_f32_16x16x32_bf16 v[110:113], v[134:137], v[170:173], v[110:113]
	v_mfma_f32_16x16x32_bf16 v[106:109], v[70:73], v[134:137], v[106:109]
	v_or_b32_e32 v136, 0x50, v199
	v_cndmask_b32_e64 v137, v196, v136, s[6:7]
	s_nop 4
	v_pk_fma_f32 v[176:177], v[112:113], 2.0, v[176:177] op_sel_hi:[1,0,1]
	v_pk_fma_f32 v[134:135], v[110:111], 2.0, v[174:175] op_sel_hi:[1,0,1]
	v_mfma_f32_16x16x32_bf16 v[110:113], v[18:21], v[170:173], v[130:133]
	s_nop 2
	v_lshl_or_b32 v130, v137, 2, v198
	ds_write_b32 v130, v134
	v_cndmask_b32_e64 v130, v196, v136, s[4:5]
	v_lshl_or_b32 v130, v130, 2, v198
	v_mfma_f32_16x16x32_bf16 v[106:109], v[66:69], v[170:173], v[106:109]
	ds_write_b32 v130, v135
	v_cndmask_b32_e64 v130, v196, v136, s[2:3]
	v_lshl_or_b32 v130, v130, 2, v198
	ds_write_b32 v130, v176
	v_cndmask_b32_e32 v130, v196, v136, vcc
	v_lshl_or_b32 v130, v130, 2, v198
	ds_write_b32 v130, v177
	ds_read_b128 v[130:133], v197 offset:4608
	ds_read_b128 v[134:137], v197 offset:4672
	ds_read_b128 v[170:173], v197 offset:4736
	ds_read_b128 v[174:177], v197 offset:4800
	s_waitcnt vmcnt(15)
	ds_write_b128 v200, v[138:141]
	s_waitcnt vmcnt(14)
	ds_write_b128 v200, v[142:145] offset:1152
	s_waitcnt vmcnt(13)
	ds_write_b128 v200, v[178:181] offset:2304
	s_waitcnt vmcnt(12)
	ds_write_b128 v200, v[182:185] offset:3456
	s_waitcnt lgkmcnt(7)
	v_cvt_pk_bf16_f32 v138, v130, v131
	v_cvt_pk_bf16_f32 v139, v132, v133
	s_waitcnt lgkmcnt(6)
	v_cvt_pk_bf16_f32 v140, v134, v135
	v_cvt_pk_bf16_f32 v141, v136, v137
	v_lshlrev_b32_e32 v142, 16, v138
	v_and_b32_e32 v143, 0xffff0000, v138
	v_mfma_f32_16x16x32_bf16 v[110:113], v[6:9], v[138:141], v[110:113]
	v_add_f32_e64 v130, v130, -v142
	v_add_f32_e64 v131, v131, -v143
	v_lshlrev_b32_e32 v142, 16, v139
	v_and_b32_e32 v143, 0xffff0000, v139
	v_mfma_f32_16x16x32_bf16 v[106:109], v[50:53], v[138:141], v[106:109]
	v_add_f32_e64 v132, v132, -v142
	v_add_f32_e64 v133, v133, -v143
	v_cvt_pk_bf16_f32 v130, v130, v131
	v_cvt_pk_bf16_f32 v131, v132, v133
	v_lshlrev_b32_e32 v132, 16, v140
	v_and_b32_e32 v133, 0xffff0000, v140
	v_mfma_f32_16x16x32_bf16 v[110:113], v[14:17], v[138:141], v[110:113]
	v_add_f32_e64 v132, v134, -v132
	v_add_f32_e64 v133, v135, -v133
	v_lshlrev_b32_e32 v134, 16, v141
	v_and_b32_e32 v135, 0xffff0000, v141
	v_mfma_f32_16x16x32_bf16 v[106:109], v[54:57], v[138:141], v[106:109]
	v_add_f32_e64 v134, v136, -v134
	v_add_f32_e64 v135, v137, -v135
	v_cvt_pk_bf16_f32 v132, v132, v133
	v_cvt_pk_bf16_f32 v133, v134, v135
	v_mfma_f32_16x16x32_bf16 v[142:145], v[138:141], v[138:141], 0
	s_nop 0
	v_mfma_f32_16x16x32_bf16 v[134:137], v[138:141], v[130:133], 0
	s_waitcnt lgkmcnt(5)
	v_cvt_pk_bf16_f32 v138, v170, v171
	v_lshlrev_b32_e32 v140, 16, v138
	v_and_b32_e32 v141, 0xffff0000, v138
	v_mfma_f32_16x16x32_bf16 v[110:113], v[6:9], v[130:133], v[110:113]
	v_cvt_pk_bf16_f32 v139, v172, v173
	v_mfma_f32_16x16x32_bf16 v[106:109], v[50:53], v[130:133], v[106:109]
	v_add_f32_e64 v130, v170, -v140
	v_add_f32_e64 v131, v171, -v141
	s_waitcnt lgkmcnt(4)
	v_cvt_pk_bf16_f32 v140, v174, v175
	v_cvt_pk_bf16_f32 v141, v176, v177
	v_lshlrev_b32_e32 v132, 16, v139
	v_and_b32_e32 v133, 0xffff0000, v139
	v_pk_add_f32 v[132:133], v[172:173], v[132:133] neg_lo:[0,1] neg_hi:[0,1]
	v_cvt_pk_bf16_f32 v130, v130, v131
	v_cvt_pk_bf16_f32 v131, v132, v133
	v_lshlrev_b32_e32 v132, 16, v140
	v_and_b32_e32 v133, 0xffff0000, v140
	v_lshlrev_b32_e32 v170, 16, v141
	v_and_b32_e32 v171, 0xffff0000, v141
	v_mfma_f32_16x16x32_bf16 v[110:113], v[2:5], v[138:141], v[110:113]
	v_add_f32_e64 v132, v174, -v132
	v_add_f32_e64 v133, v175, -v133
	v_pk_add_f32 v[170:171], v[176:177], v[170:171] neg_lo:[0,1] neg_hi:[0,1]
	v_cvt_pk_bf16_f32 v132, v132, v133
	v_cvt_pk_bf16_f32 v133, v170, v171
	v_mfma_f32_16x16x32_bf16 v[106:109], v[42:45], v[138:141], v[106:109]
	v_mfma_f32_16x16x32_bf16 v[142:145], v[138:141], v[138:141], v[142:145]
	v_mfma_f32_16x16x32_bf16 v[134:137], v[138:141], v[130:133], v[134:137]
	v_mfma_f32_16x16x32_bf16 v[110:113], v[10:13], v[138:141], v[110:113]
	s_nop 6
	v_fma_f32 v144, v136, 2.0, v144
	v_fma_f32 v145, v137, 2.0, v145
	v_mfma_f32_16x16x32_bf16 v[136:139], v[46:49], v[138:141], v[106:109]
	v_or_b32_e32 v140, 0xd0, v199
	v_cndmask_b32_e64 v141, v196, v140, s[6:7]
	v_pk_fma_f32 v[134:135], v[134:135], 2.0, v[142:143] op_sel_hi:[1,0,1]
	v_mfma_f32_16x16x32_bf16 v[106:109], v[2:5], v[130:133], v[110:113]
	s_nop 2
	v_lshl_or_b32 v110, v141, 2, v198
	ds_write_b32 v110, v134
	v_cndmask_b32_e64 v134, v196, v140, s[4:5]
	v_mfma_f32_16x16x32_bf16 v[110:113], v[42:45], v[130:133], v[136:139]
	v_lshl_or_b32 v130, v134, 2, v198
	ds_write_b32 v130, v135
	v_cndmask_b32_e64 v130, v196, v140, s[2:3]
	v_lshl_or_b32 v130, v130, 2, v198
	ds_write_b32 v130, v144
	v_cndmask_b32_e32 v130, v196, v140, vcc
	v_lshl_or_b32 v130, v130, 2, v198
	ds_write_b32 v130, v145
	ds_read_b128 v[130:133], v197
	ds_read_b128 v[134:137], v197 offset:64
	ds_read_b128 v[138:141], v197 offset:128
	ds_read_b128 v[142:145], v197 offset:192
	s_waitcnt vmcnt(11)
	ds_write_b128 v200, v[146:149] offset:4608
	s_waitcnt vmcnt(10)
	ds_write_b128 v200, v[150:153] offset:5760
	s_waitcnt vmcnt(9)
	ds_write_b128 v200, v[186:189] offset:6912
	s_waitcnt vmcnt(8)
	ds_write_b128 v200, v[190:193] offset:8064
	s_waitcnt lgkmcnt(7)
	v_cvt_pk_bf16_f32 v146, v130, v131
	v_cvt_pk_bf16_f32 v147, v132, v133
	s_waitcnt lgkmcnt(6)
	v_cvt_pk_bf16_f32 v148, v134, v135
	v_cvt_pk_bf16_f32 v149, v136, v137
	v_lshlrev_b32_e32 v170, 16, v146
	v_and_b32_e32 v171, 0xffff0000, v146
	v_mfma_f32_16x16x32_bf16 v[150:153], v[22:25], v[146:149], 0
	v_add_f32_e64 v130, v130, -v170
	v_add_f32_e64 v131, v131, -v171
	v_lshlrev_b32_e32 v174, 16, v147
	v_and_b32_e32 v175, 0xffff0000, v147
	v_mfma_f32_16x16x32_bf16 v[170:173], v[34:37], v[146:149], 0
	v_add_f32_e64 v132, v132, -v174
	v_add_f32_e64 v133, v133, -v175
	v_cvt_pk_bf16_f32 v130, v130, v131
	v_cvt_pk_bf16_f32 v131, v132, v133
	v_lshlrev_b32_e32 v132, 16, v148
	v_and_b32_e32 v133, 0xffff0000, v148
	v_mfma_f32_16x16x32_bf16 v[150:153], v[30:33], v[146:149], v[150:153]
	v_add_f32_e64 v132, v134, -v132
	v_add_f32_e64 v133, v135, -v133
	v_lshlrev_b32_e32 v134, 16, v149
	v_and_b32_e32 v135, 0xffff0000, v149
	v_mfma_f32_16x16x32_bf16 v[170:173], v[38:41], v[146:149], v[170:173]
	v_add_f32_e64 v134, v136, -v134
	v_add_f32_e64 v135, v137, -v135
	v_cvt_pk_bf16_f32 v132, v132, v133
	v_cvt_pk_bf16_f32 v133, v134, v135
	v_mfma_f32_16x16x32_bf16 v[174:177], v[146:149], v[146:149], 0
	s_nop 0
	v_mfma_f32_16x16x32_bf16 v[134:137], v[146:149], v[130:133], 0
	v_mfma_f32_16x16x32_bf16 v[146:149], v[22:25], v[130:133], v[150:153]
	s_waitcnt lgkmcnt(5)
	s_nop 1
	v_cvt_pk_bf16_f32 v150, v138, v139
	v_cvt_pk_bf16_f32 v151, v140, v141
	v_lshlrev_b32_e32 v152, 16, v150
	v_and_b32_e32 v153, 0xffff0000, v150
	v_mfma_f32_16x16x32_bf16 v[130:133], v[34:37], v[130:133], v[170:173]
	v_add_f32_e64 v138, v138, -v152
	v_add_f32_e64 v139, v139, -v153
	s_waitcnt lgkmcnt(4)
	v_cvt_pk_bf16_f32 v152, v142, v143
	v_cvt_pk_bf16_f32 v153, v144, v145
	v_lshlrev_b32_e32 v170, 16, v151
	v_and_b32_e32 v171, 0xffff0000, v151
	v_pk_add_f32 v[140:141], v[140:141], v[170:171] neg_lo:[0,1] neg_hi:[0,1]
	v_cvt_pk_bf16_f32 v138, v138, v139
	v_mfma_f32_16x16x32_bf16 v[146:149], v[18:21], v[150:153], v[146:149]
	v_cvt_pk_bf16_f32 v139, v140, v141
	v_lshlrev_b32_e32 v140, 16, v152
	v_and_b32_e32 v141, 0xffff0000, v152
	v_pk_add_f32 v[140:141], v[142:143], v[140:141] neg_lo:[0,1] neg_hi:[0,1]
	v_lshlrev_b32_e32 v142, 16, v153
	v_and_b32_e32 v143, 0xffff0000, v153
	v_mfma_f32_16x16x32_bf16 v[130:133], v[66:69], v[150:153], v[130:133]
	v_add_f32_e64 v142, v144, -v142
	v_add_f32_e64 v143, v145, -v143
	v_cvt_pk_bf16_f32 v140, v140, v141
	v_cvt_pk_bf16_f32 v141, v142, v143
	v_mfma_f32_16x16x32_bf16 v[170:173], v[150:153], v[150:153], v[174:177]
	v_mfma_f32_16x16x32_bf16 v[146:149], v[26:29], v[150:153], v[146:149]
	v_mfma_f32_16x16x32_bf16 v[134:137], v[150:153], v[138:141], v[134:137]
	v_mfma_f32_16x16x32_bf16 v[130:133], v[70:73], v[150:153], v[130:133]
	v_or_b32_e32 v150, 0x60, v199
	v_cndmask_b32_e64 v151, v196, v150, s[6:7]
	s_nop 4
	v_pk_fma_f32 v[142:143], v[136:137], 2.0, v[172:173] op_sel_hi:[1,0,1]
	v_pk_fma_f32 v[144:145], v[134:135], 2.0, v[170:171] op_sel_hi:[1,0,1]
	v_mfma_f32_16x16x32_bf16 v[134:137], v[18:21], v[138:141], v[146:149]
	s_nop 2
	v_lshl_or_b32 v146, v151, 2, v198
	ds_write_b32 v146, v144
	v_cndmask_b32_e64 v144, v196, v150, s[4:5]
	v_mfma_f32_16x16x32_bf16 v[130:133], v[66:69], v[138:141], v[130:133]
	v_lshl_or_b32 v138, v144, 2, v198
	ds_write_b32 v138, v145
	v_cndmask_b32_e64 v138, v196, v150, s[2:3]
	v_lshl_or_b32 v138, v138, 2, v198
	ds_write_b32 v138, v142
	v_cndmask_b32_e32 v138, v196, v150, vcc
	v_lshl_or_b32 v138, v138, 2, v198
	ds_write_b32 v138, v143
	ds_read_b128 v[138:141], v197 offset:4608
	ds_read_b128 v[142:145], v197 offset:4672
	ds_read_b128 v[146:149], v197 offset:4736
	ds_read_b128 v[150:153], v197 offset:4800
	s_waitcnt vmcnt(7)
	ds_write_b128 v200, v[114:117]
	s_waitcnt vmcnt(6)
	ds_write_b128 v200, v[118:121] offset:1152
	s_waitcnt vmcnt(5)
	ds_write_b128 v200, v[154:157] offset:2304
	s_waitcnt vmcnt(4)
	ds_write_b128 v200, v[158:161] offset:3456
	s_waitcnt lgkmcnt(7)
	v_cvt_pk_bf16_f32 v114, v138, v139
	v_cvt_pk_bf16_f32 v115, v140, v141
	s_waitcnt lgkmcnt(6)
	v_cvt_pk_bf16_f32 v116, v142, v143
	v_cvt_pk_bf16_f32 v117, v144, v145
	v_lshlrev_b32_e32 v154, 16, v114
	v_and_b32_e32 v155, 0xffff0000, v114
	v_mfma_f32_16x16x32_bf16 v[118:121], v[6:9], v[114:117], v[134:137]
	v_mfma_f32_16x16x32_bf16 v[130:133], v[50:53], v[114:117], v[130:133]
	s_nop 1
	v_lshlrev_b32_e32 v136, 16, v115
	v_and_b32_e32 v137, 0xffff0000, v115
	v_pk_add_f32 v[134:135], v[138:139], v[154:155] neg_lo:[0,1] neg_hi:[0,1]
	v_pk_add_f32 v[136:137], v[140:141], v[136:137] neg_lo:[0,1] neg_hi:[0,1]
	v_cvt_pk_bf16_f32 v134, v134, v135
	v_cvt_pk_bf16_f32 v135, v136, v137
	v_lshlrev_b32_e32 v136, 16, v116
	v_and_b32_e32 v137, 0xffff0000, v116
	v_mfma_f32_16x16x32_bf16 v[118:121], v[14:17], v[114:117], v[118:121]
	v_add_f32_e64 v136, v142, -v136
	v_add_f32_e64 v137, v143, -v137
	v_lshlrev_b32_e32 v142, 16, v117
	v_and_b32_e32 v143, 0xffff0000, v117
	v_mfma_f32_16x16x32_bf16 v[130:133], v[54:57], v[114:117], v[130:133]
	v_add_f32_e64 v142, v144, -v142
	v_add_f32_e64 v143, v145, -v143
	v_cvt_pk_bf16_f32 v136, v136, v137
	v_cvt_pk_bf16_f32 v137, v142, v143
	s_waitcnt lgkmcnt(5)
	v_cvt_pk_bf16_f32 v142, v146, v147
	v_lshlrev_b32_e32 v144, 16, v142
	v_mfma_f32_16x16x32_bf16 v[118:121], v[6:9], v[134:137], v[118:121]
	v_and_b32_e32 v145, 0xffff0000, v142
	v_cvt_pk_bf16_f32 v143, v148, v149
	v_mfma_f32_16x16x32_bf16 v[130:133], v[50:53], v[134:137], v[130:133]
	v_mfma_f32_16x16x32_bf16 v[138:141], v[114:117], v[114:117], 0
	v_mfma_f32_16x16x32_bf16 v[114:117], v[114:117], v[134:137], 0
	v_add_f32_e64 v134, v146, -v144
	v_add_f32_e64 v135, v147, -v145
	s_waitcnt lgkmcnt(4)
	v_cvt_pk_bf16_f32 v144, v150, v151
	v_cvt_pk_bf16_f32 v145, v152, v153
	v_lshlrev_b32_e32 v136, 16, v143
	v_and_b32_e32 v137, 0xffff0000, v143
	v_mfma_f32_16x16x32_bf16 v[118:121], v[2:5], v[142:145], v[118:121]
	v_add_f32_e64 v136, v148, -v136
	v_add_f32_e64 v137, v149, -v137
	v_cvt_pk_bf16_f32 v134, v134, v135
	v_cvt_pk_bf16_f32 v135, v136, v137
	v_lshlrev_b32_e32 v136, 16, v144
	v_and_b32_e32 v137, 0xffff0000, v144
	v_lshlrev_b32_e32 v146, 16, v145
	v_and_b32_e32 v147, 0xffff0000, v145
	v_mfma_f32_16x16x32_bf16 v[130:133], v[42:45], v[142:145], v[130:133]
	v_add_f32_e64 v136, v150, -v136
	v_add_f32_e64 v137, v151, -v137
	v_pk_add_f32 v[146:147], v[152:153], v[146:147] neg_lo:[0,1] neg_hi:[0,1]
	v_cvt_pk_bf16_f32 v136, v136, v137
	v_cvt_pk_bf16_f32 v137, v146, v147
	v_mfma_f32_16x16x32_bf16 v[138:141], v[142:145], v[142:145], v[138:141]
	v_mfma_f32_16x16x32_bf16 v[118:121], v[10:13], v[142:145], v[118:121]
	v_mfma_f32_16x16x32_bf16 v[114:117], v[142:145], v[134:137], v[114:117]
	v_mfma_f32_16x16x32_bf16 v[130:133], v[46:49], v[142:145], v[130:133]
	v_or_b32_e32 v142, 0xe0, v199
	v_cndmask_b32_e64 v143, v196, v142, s[6:7]
	s_nop 4
	v_pk_fma_f32 v[140:141], v[116:117], 2.0, v[140:141] op_sel_hi:[1,0,1]
	v_pk_fma_f32 v[138:139], v[114:115], 2.0, v[138:139] op_sel_hi:[1,0,1]
	v_mfma_f32_16x16x32_bf16 v[114:117], v[2:5], v[134:137], v[118:121]
	s_nop 2
	v_lshl_or_b32 v118, v143, 2, v198
	ds_write_b32 v118, v138
	v_cndmask_b32_e64 v138, v196, v142, s[4:5]
	v_mfma_f32_16x16x32_bf16 v[118:121], v[42:45], v[134:137], v[130:133]
	s_nop 2
	v_lshl_or_b32 v130, v138, 2, v198
	ds_write_b32 v130, v139
	v_cndmask_b32_e64 v130, v196, v142, s[2:3]
	v_lshl_or_b32 v130, v130, 2, v198
	ds_write_b32 v130, v140
	v_cndmask_b32_e32 v130, v196, v142, vcc
	v_lshl_or_b32 v130, v130, 2, v198
	ds_write_b32 v130, v141
	ds_read_b128 v[130:133], v197
	ds_read_b128 v[134:137], v197 offset:64
	ds_read_b128 v[138:141], v197 offset:128
	ds_read_b128 v[142:145], v197 offset:192
	s_waitcnt vmcnt(3)
	ds_write_b128 v200, v[122:125] offset:4608
	s_waitcnt vmcnt(2)
	ds_write_b128 v200, v[126:129] offset:5760
	s_waitcnt vmcnt(1)
	ds_write_b128 v200, v[162:165] offset:6912
	s_waitcnt vmcnt(0)
	ds_write_b128 v200, v[166:169] offset:8064
	s_waitcnt lgkmcnt(7)
	v_cvt_pk_bf16_f32 v122, v130, v131
	v_cvt_pk_bf16_f32 v123, v132, v133
	s_waitcnt lgkmcnt(6)
	v_cvt_pk_bf16_f32 v124, v134, v135
	v_cvt_pk_bf16_f32 v125, v136, v137
	v_lshlrev_b32_e32 v146, 16, v122
	v_and_b32_e32 v147, 0xffff0000, v122
	v_mfma_f32_16x16x32_bf16 v[126:129], v[22:25], v[122:125], 0
	v_lshlrev_b32_e32 v150, 16, v123
	v_and_b32_e32 v151, 0xffff0000, v123
	v_pk_add_f32 v[130:131], v[130:131], v[146:147] neg_lo:[0,1] neg_hi:[0,1]
	v_pk_add_f32 v[132:133], v[132:133], v[150:151] neg_lo:[0,1] neg_hi:[0,1]
	v_cvt_pk_bf16_f32 v130, v130, v131
	v_mfma_f32_16x16x32_bf16 v[146:149], v[34:37], v[122:125], 0
	v_cvt_pk_bf16_f32 v131, v132, v133
	v_lshlrev_b32_e32 v132, 16, v124
	v_and_b32_e32 v133, 0xffff0000, v124
	v_mfma_f32_16x16x32_bf16 v[30:33], v[30:33], v[122:125], v[126:129]
	s_nop 2
	v_add_f32_e64 v126, v134, -v132
	v_add_f32_e64 v127, v135, -v133
	v_mfma_f32_16x16x32_bf16 v[38:41], v[38:41], v[122:125], v[146:149]
	v_cvt_pk_bf16_f32 v132, v126, v127
	v_lshlrev_b32_e32 v126, 16, v125
	v_and_b32_e32 v127, 0xffff0000, v125
	v_pk_add_f32 v[126:127], v[136:137], v[126:127] neg_lo:[0,1] neg_hi:[0,1]
	v_mfma_f32_16x16x32_bf16 v[150:153], v[122:125], v[122:125], 0
	v_cvt_pk_bf16_f32 v133, v126, v127
	s_nop 1
	v_mfma_f32_16x16x32_bf16 v[22:25], v[22:25], v[130:133], v[30:33]
	s_waitcnt lgkmcnt(5)
	s_nop 1
	v_cvt_pk_bf16_f32 v30, v138, v139
	v_lshlrev_b32_e32 v32, 16, v30
	v_and_b32_e32 v33, 0xffff0000, v30
	v_pk_add_f32 v[32:33], v[138:139], v[32:33] neg_lo:[0,1] neg_hi:[0,1]
	v_mfma_f32_16x16x32_bf16 v[34:37], v[34:37], v[130:133], v[38:41]
	v_cvt_pk_bf16_f32 v31, v140, v141
	s_nop 1
	v_cvt_pk_bf16_f32 v38, v32, v33
	s_waitcnt lgkmcnt(4)
	v_cvt_pk_bf16_f32 v32, v142, v143
	v_cvt_pk_bf16_f32 v33, v144, v145
	v_lshlrev_b32_e32 v40, 16, v31
	v_and_b32_e32 v41, 0xffff0000, v31
	v_mfma_f32_16x16x32_bf16 v[22:25], v[18:21], v[30:33], v[22:25]
	v_add_f32_e64 v40, v140, -v40
	v_add_f32_e64 v41, v141, -v41
	v_cvt_pk_bf16_f32 v39, v40, v41
	v_mfma_f32_16x16x32_bf16 v[122:125], v[122:125], v[130:133], 0
	v_lshlrev_b32_e32 v40, 16, v32
	v_and_b32_e32 v41, 0xffff0000, v32
	v_lshlrev_b32_e32 v130, 16, v33
	v_and_b32_e32 v131, 0xffff0000, v33
	v_pk_add_f32 v[40:41], v[142:143], v[40:41] neg_lo:[0,1] neg_hi:[0,1]
	v_mfma_f32_16x16x32_bf16 v[22:25], v[26:29], v[30:33], v[22:25]
	v_add_f32_e64 v26, v144, -v130
	v_add_f32_e64 v27, v145, -v131
	v_cvt_pk_bf16_f32 v40, v40, v41
	v_cvt_pk_bf16_f32 v41, v26, v27
	v_mfma_f32_16x16x32_bf16 v[34:37], v[66:69], v[30:33], v[34:37]
	v_mfma_f32_16x16x32_bf16 v[126:129], v[30:33], v[30:33], v[150:153]
	v_mfma_f32_16x16x32_bf16 v[26:29], v[30:33], v[38:41], v[122:125]
	v_mfma_f32_16x16x32_bf16 v[18:21], v[18:21], v[38:41], v[22:25]
	s_nop 6
	v_fma_f32 v122, v28, 2.0, v128
	v_fma_f32 v123, v29, 2.0, v129
	v_mfma_f32_16x16x32_bf16 v[28:31], v[70:73], v[30:33], v[34:37]
	v_or_b32_e32 v32, 0x70, v199
	v_cndmask_b32_e64 v33, v196, v32, s[6:7]
	v_pk_fma_f32 v[26:27], v[26:27], 2.0, v[126:127] op_sel_hi:[1,0,1]
	v_lshl_or_b32 v22, v33, 2, v198
	ds_write_b32 v22, v26
	v_cndmask_b32_e64 v26, v196, v32, s[4:5]
	v_lshl_or_b32 v26, v26, 2, v198
	ds_write_b32 v26, v27
	v_cndmask_b32_e64 v26, v196, v32, s[2:3]
	v_lshl_or_b32 v26, v26, 2, v198
	ds_write_b32 v26, v122
	v_cndmask_b32_e32 v26, v196, v32, vcc
	v_lshl_or_b32 v26, v26, 2, v198
	v_mfma_f32_16x16x32_bf16 v[22:25], v[66:69], v[38:41], v[28:31]
	ds_write_b32 v26, v123
	s_nop 1
	ds_read_b128 v[26:29], v197 offset:4608
	ds_read_b128 v[30:33], v197 offset:4672
	ds_read_b128 v[34:37], v197 offset:4736
	ds_read_b128 v[38:41], v197 offset:4800
	s_waitcnt lgkmcnt(3)
	v_cvt_pk_bf16_f32 v66, v26, v27
	v_cvt_pk_bf16_f32 v67, v28, v29
	s_waitcnt lgkmcnt(2)
	v_cvt_pk_bf16_f32 v68, v30, v31
	v_cvt_pk_bf16_f32 v69, v32, v33
	v_lshlrev_b32_e32 v70, 16, v66
	v_and_b32_e32 v71, 0xffff0000, v66
	v_mfma_f32_16x16x32_bf16 v[18:21], v[6:9], v[66:69], v[18:21]
	v_add_f32_e64 v26, v26, -v70
	v_add_f32_e64 v27, v27, -v71
	v_lshlrev_b32_e32 v70, 16, v67
	v_and_b32_e32 v71, 0xffff0000, v67
	v_mfma_f32_16x16x32_bf16 v[22:25], v[50:53], v[66:69], v[22:25]
	v_add_f32_e64 v28, v28, -v70
	v_add_f32_e64 v29, v29, -v71
	v_cvt_pk_bf16_f32 v26, v26, v27
	v_cvt_pk_bf16_f32 v27, v28, v29
	v_lshlrev_b32_e32 v28, 16, v68
	v_and_b32_e32 v29, 0xffff0000, v68
	v_mfma_f32_16x16x32_bf16 v[14:17], v[14:17], v[66:69], v[18:21]
	s_nop 2
	v_add_f32_e64 v18, v30, -v28
	v_add_f32_e64 v19, v31, -v29
	v_lshlrev_b32_e32 v30, 16, v69
	v_and_b32_e32 v31, 0xffff0000, v69
	v_cvt_pk_bf16_f32 v28, v18, v19
	v_mfma_f32_16x16x32_bf16 v[18:21], v[54:57], v[66:69], v[22:25]
	s_nop 2
	v_add_f32_e64 v22, v32, -v30
	v_add_f32_e64 v23, v33, -v31
	v_mfma_f32_16x16x32_bf16 v[70:73], v[66:69], v[66:69], 0
	v_cvt_pk_bf16_f32 v29, v22, v23
	s_nop 1
	v_mfma_f32_16x16x32_bf16 v[6:9], v[6:9], v[26:29], v[14:17]
	s_waitcnt lgkmcnt(1)
	s_nop 1
	v_cvt_pk_bf16_f32 v14, v34, v35
	v_lshlrev_b32_e32 v16, 16, v14
	v_and_b32_e32 v17, 0xffff0000, v14
	v_pk_add_f32 v[16:17], v[34:35], v[16:17] neg_lo:[0,1] neg_hi:[0,1]
	v_mfma_f32_16x16x32_bf16 v[22:25], v[66:69], v[26:29], 0
	v_cvt_pk_bf16_f32 v15, v36, v37
	v_mfma_f32_16x16x32_bf16 v[18:21], v[50:53], v[26:29], v[18:21]
	v_cvt_pk_bf16_f32 v26, v16, v17
	s_waitcnt lgkmcnt(0)
	v_cvt_pk_bf16_f32 v16, v38, v39
	v_cvt_pk_bf16_f32 v17, v40, v41
	v_lshlrev_b32_e32 v28, 16, v15
	v_and_b32_e32 v29, 0xffff0000, v15
	v_mfma_f32_16x16x32_bf16 v[6:9], v[2:5], v[14:17], v[6:9]
	v_add_f32_e64 v28, v36, -v28
	v_add_f32_e64 v29, v37, -v29
	v_lshlrev_b32_e32 v34, 16, v17
	v_cvt_pk_bf16_f32 v27, v28, v29
	v_lshlrev_b32_e32 v28, 16, v16
	v_and_b32_e32 v29, 0xffff0000, v16
	v_and_b32_e32 v35, 0xffff0000, v17
	v_pk_add_f32 v[28:29], v[38:39], v[28:29] neg_lo:[0,1] neg_hi:[0,1]
	v_mfma_f32_16x16x32_bf16 v[6:9], v[10:13], v[14:17], v[6:9]
	v_add_f32_e64 v10, v40, -v34
	v_add_f32_e64 v11, v41, -v35
	v_cvt_pk_bf16_f32 v28, v28, v29
	v_cvt_pk_bf16_f32 v29, v10, v11
	v_mfma_f32_16x16x32_bf16 v[18:21], v[42:45], v[14:17], v[18:21]
	v_mfma_f32_16x16x32_bf16 v[30:33], v[14:17], v[14:17], v[70:73]
	v_mfma_f32_16x16x32_bf16 v[10:13], v[14:17], v[26:29], v[22:25]
	v_mfma_f32_16x16x32_bf16 v[2:5], v[2:5], v[26:29], v[6:9]
	s_nop 6
	v_fma_f32 v22, v12, 2.0, v32
	v_fma_f32 v23, v13, 2.0, v33
	v_mfma_f32_16x16x32_bf16 v[12:15], v[46:49], v[14:17], v[18:21]
	v_or_b32_e32 v16, 0xf0, v199
	v_cndmask_b32_e64 v17, v196, v16, s[6:7]
	v_pk_fma_f32 v[10:11], v[10:11], 2.0, v[30:31] op_sel_hi:[1,0,1]
	v_lshl_or_b32 v6, v17, 2, v198
	ds_write_b32 v6, v10
	v_cndmask_b32_e64 v10, v196, v16, s[4:5]
	v_lshl_or_b32 v10, v10, 2, v198
	v_mfma_f32_16x16x32_bf16 v[6:9], v[42:45], v[26:29], v[12:15]
	ds_write_b32 v10, v11
	v_cndmask_b32_e64 v10, v196, v16, s[2:3]
	v_lshl_or_b32 v10, v10, 2, v198
	ds_write_b32 v10, v22
	v_cndmask_b32_e32 v10, v196, v16, vcc
	v_lshl_or_b32 v10, v10, 2, v198
	ds_write_b32 v10, v23
